# v106 with every GEMM MFMA block padded to start at an address that is 0 mod 8 (8-byte MFMAs never straddle an 8-byte fetch boundary)
# baseline (speedup 1.0000x reference)
.LBB0_114:
	ds_read_b128 v[130:133], v220
	ds_read_b128 v[134:137], v220 offset:1024
	ds_read_b128 v[138:141], v220 offset:2048
	ds_read_b128 v[142:145], v220 offset:3072
	ds_read_b128 v[146:149], v221
	ds_read_b128 v[150:153], v221 offset:1024
	ds_read_b128 v[154:157], v221 offset:2048
	ds_read_b128 v[158:161], v221 offset:3072
	s_add_i32 s46, s64, 0xfff80080
	s_cmp_eq_u32 s84, 28
	s_cselect_b32 s87, s62, s46
	s_cselect_b32 s86, s63, s65
	s_or_b32 s85, s87, 0x80
	s_mov_b32 m0, s93
	ds_read_b128 v[162:165], v222
	ds_read_b128 v[166:169], v222 offset:1024
	ds_read_b128 v[170:173], v222 offset:2048
	ds_read_b128 v[174:177], v222 offset:3072
	ds_read_b128 v[178:181], v222 offset:4096
	ds_read_b128 v[182:185], v222 offset:5120
	ds_read_b128 v[186:189], v222 offset:6144
	ds_read_b128 v[212:215], v222 offset:7168
	buffer_load_dwordx4 v1, s[40:43], s64 offen lds
	s_mov_b32 m0, s94
	s_nop 0
	buffer_load_dwordx4 v216, s[40:43], s64 offen lds
	s_waitcnt vmcnt(8)
	s_waitcnt lgkmcnt(0)
	s_nop 0
	s_barrier
	v_mfma_f32_16x16x32_bf16 v[126:129], v[130:133], v[162:165], v[126:129]
	v_mfma_f32_16x16x32_bf16 v[126:129], v[134:137], v[166:169], v[126:129]
	v_mfma_f32_16x16x32_bf16 v[122:125], v[142:145], v[166:169], v[122:125]
	v_mfma_f32_16x16x32_bf16 v[122:125], v[138:141], v[162:165], v[122:125]
	v_mfma_f32_16x16x32_bf16 v[106:109], v[138:141], v[170:173], v[106:109]
	v_mfma_f32_16x16x32_bf16 v[106:109], v[142:145], v[174:177], v[106:109]
	v_mfma_f32_16x16x32_bf16 v[114:117], v[134:137], v[174:177], v[114:117]
	v_mfma_f32_16x16x32_bf16 v[114:117], v[130:133], v[170:173], v[114:117]
	v_mfma_f32_16x16x32_bf16 v[102:105], v[130:133], v[178:181], v[102:105]
	v_mfma_f32_16x16x32_bf16 v[102:105], v[134:137], v[182:185], v[102:105]
	v_mfma_f32_16x16x32_bf16 v[94:97], v[142:145], v[182:185], v[94:97]
	v_mfma_f32_16x16x32_bf16 v[94:97], v[138:141], v[178:181], v[94:97]
	v_mfma_f32_16x16x32_bf16 v[78:81], v[138:141], v[186:189], v[78:81]
	v_mfma_f32_16x16x32_bf16 v[78:81], v[142:145], v[212:215], v[78:81]
	v_mfma_f32_16x16x32_bf16 v[86:89], v[134:137], v[212:215], v[86:89]
	v_mfma_f32_16x16x32_bf16 v[86:89], v[130:133], v[186:189], v[86:89]
	v_mfma_f32_16x16x32_bf16 v[118:121], v[146:149], v[162:165], v[118:121]
	v_mfma_f32_16x16x32_bf16 v[118:121], v[150:153], v[166:169], v[118:121]
	v_mfma_f32_16x16x32_bf16 v[110:113], v[158:161], v[166:169], v[110:113]
	v_mfma_f32_16x16x32_bf16 v[110:113], v[154:157], v[162:165], v[110:113]
	v_mfma_f32_16x16x32_bf16 v[90:93], v[154:157], v[170:173], v[90:93]
	v_mfma_f32_16x16x32_bf16 v[90:93], v[158:161], v[174:177], v[90:93]
	v_mfma_f32_16x16x32_bf16 v[98:101], v[150:153], v[174:177], v[98:101]
	v_mfma_f32_16x16x32_bf16 v[98:101], v[146:149], v[170:173], v[98:101]
	v_mfma_f32_16x16x32_bf16 v[82:85], v[146:149], v[178:181], v[82:85]
	v_mfma_f32_16x16x32_bf16 v[82:85], v[150:153], v[182:185], v[82:85]
	v_mfma_f32_16x16x32_bf16 v[74:77], v[158:161], v[182:185], v[74:77]
	v_mfma_f32_16x16x32_bf16 v[74:77], v[154:157], v[178:181], v[74:77]
	v_mfma_f32_16x16x32_bf16 v[66:69], v[154:157], v[186:189], v[66:69]
	v_mfma_f32_16x16x32_bf16 v[66:69], v[158:161], v[212:215], v[66:69]
	v_mfma_f32_16x16x32_bf16 v[70:73], v[150:153], v[212:215], v[70:73]
	v_mfma_f32_16x16x32_bf16 v[70:73], v[146:149], v[186:189], v[70:73]
	s_barrier
	s_mov_b32 m0, s69
	s_mov_b32 s46, s42
	s_mov_b32 s47, s43
	ds_read_b128 v[162:165], v222 offset:16384
	ds_read_b128 v[166:169], v222 offset:17408
	ds_read_b128 v[170:173], v222 offset:18432
	ds_read_b128 v[174:177], v222 offset:19456
	ds_read_b128 v[178:181], v222 offset:20480
	ds_read_b128 v[182:185], v222 offset:21504
	ds_read_b128 v[186:189], v222 offset:22528
	ds_read_b128 v[212:215], v222 offset:23552
	buffer_load_dwordx4 v191, s[44:47], s86 offen lds
	s_mov_b32 m0, s70
	s_add_i32 s88, s86, 0x80000
	buffer_load_dwordx4 v217, s[44:47], s86 offen lds
	s_mov_b32 m0, s71
	s_nop 0
	buffer_load_dwordx4 v191, s[44:47], s88 offen lds
	s_mov_b32 m0, s72
	s_nop 0
	buffer_load_dwordx4 v217, s[44:47], s88 offen lds
	s_mov_b32 m0, s68
	s_nop 0
	buffer_load_dwordx4 v1, s[40:43], s87 offen lds
	s_mov_b32 m0, s73
	s_nop 0
	buffer_load_dwordx4 v216, s[40:43], s87 offen lds
	s_waitcnt vmcnt(8)
	s_waitcnt lgkmcnt(0)
	s_barrier
	v_mfma_f32_16x16x32_bf16 v[62:65], v[130:133], v[162:165], v[62:65]
	v_mfma_f32_16x16x32_bf16 v[62:65], v[134:137], v[166:169], v[62:65]
	v_mfma_f32_16x16x32_bf16 v[58:61], v[142:145], v[166:169], v[58:61]
	v_mfma_f32_16x16x32_bf16 v[58:61], v[138:141], v[162:165], v[58:61]
	v_mfma_f32_16x16x32_bf16 v[46:49], v[138:141], v[170:173], v[46:49]
	v_mfma_f32_16x16x32_bf16 v[46:49], v[142:145], v[174:177], v[46:49]
	v_mfma_f32_16x16x32_bf16 v[54:57], v[134:137], v[174:177], v[54:57]
	v_mfma_f32_16x16x32_bf16 v[54:57], v[130:133], v[170:173], v[54:57]
	v_mfma_f32_16x16x32_bf16 v[38:41], v[130:133], v[178:181], v[38:41]
	v_mfma_f32_16x16x32_bf16 v[38:41], v[134:137], v[182:185], v[38:41]
	v_mfma_f32_16x16x32_bf16 v[30:33], v[142:145], v[182:185], v[30:33]
	v_mfma_f32_16x16x32_bf16 v[30:33], v[138:141], v[178:181], v[30:33]
	v_mfma_f32_16x16x32_bf16 v[14:17], v[138:141], v[186:189], v[14:17]
	v_mfma_f32_16x16x32_bf16 v[14:17], v[142:145], v[212:215], v[14:17]
	v_mfma_f32_16x16x32_bf16 v[22:25], v[134:137], v[212:215], v[22:25]
	v_mfma_f32_16x16x32_bf16 v[22:25], v[130:133], v[186:189], v[22:25]
	v_mfma_f32_16x16x32_bf16 v[50:53], v[146:149], v[162:165], v[50:53]
	v_mfma_f32_16x16x32_bf16 v[50:53], v[150:153], v[166:169], v[50:53]
	v_mfma_f32_16x16x32_bf16 v[42:45], v[158:161], v[166:169], v[42:45]
	v_mfma_f32_16x16x32_bf16 v[42:45], v[154:157], v[162:165], v[42:45]
	v_mfma_f32_16x16x32_bf16 v[26:29], v[154:157], v[170:173], v[26:29]
	v_mfma_f32_16x16x32_bf16 v[26:29], v[158:161], v[174:177], v[26:29]
	v_mfma_f32_16x16x32_bf16 v[34:37], v[150:153], v[174:177], v[34:37]
	v_mfma_f32_16x16x32_bf16 v[34:37], v[146:149], v[170:173], v[34:37]
	v_mfma_f32_16x16x32_bf16 v[18:21], v[146:149], v[178:181], v[18:21]
	v_mfma_f32_16x16x32_bf16 v[18:21], v[150:153], v[182:185], v[18:21]
	v_mfma_f32_16x16x32_bf16 v[10:13], v[158:161], v[182:185], v[10:13]
	v_mfma_f32_16x16x32_bf16 v[10:13], v[154:157], v[178:181], v[10:13]
	v_mfma_f32_16x16x32_bf16 v[2:5], v[154:157], v[186:189], v[2:5]
	v_mfma_f32_16x16x32_bf16 v[2:5], v[158:161], v[212:215], v[2:5]
	v_mfma_f32_16x16x32_bf16 v[6:9], v[150:153], v[212:215], v[6:9]
	v_mfma_f32_16x16x32_bf16 v[6:9], v[146:149], v[186:189], v[6:9]
	s_barrier
	ds_read_b128 v[130:133], v223
	ds_read_b128 v[134:137], v223 offset:1024
	ds_read_b128 v[138:141], v223 offset:2048
	ds_read_b128 v[142:145], v223 offset:3072
	ds_read_b128 v[146:149], v224
	ds_read_b128 v[150:153], v224 offset:1024
	ds_read_b128 v[154:157], v224 offset:2048
	ds_read_b128 v[158:161], v224 offset:3072
	s_add_i32 s87, s87, 0x80000
	s_mov_b32 m0, s74
	ds_read_b128 v[162:165], v222 offset:32768
	ds_read_b128 v[166:169], v222 offset:33792
	ds_read_b128 v[170:173], v222 offset:34816
	ds_read_b128 v[174:177], v222 offset:35840
	ds_read_b128 v[178:181], v222 offset:36864
	ds_read_b128 v[182:185], v222 offset:37888
	ds_read_b128 v[186:189], v222 offset:38912
	ds_read_b128 v[212:215], v222 offset:39936
	buffer_load_dwordx4 v1, s[40:43], s87 offen lds
	s_mov_b32 m0, s75
	s_nop 0
	buffer_load_dwordx4 v216, s[40:43], s87 offen lds
	s_waitcnt vmcnt(8)
	s_waitcnt lgkmcnt(0)
	s_nop 0
	s_barrier
	v_mfma_f32_16x16x32_bf16 v[126:129], v[130:133], v[162:165], v[126:129]
	v_mfma_f32_16x16x32_bf16 v[126:129], v[134:137], v[166:169], v[126:129]
	v_mfma_f32_16x16x32_bf16 v[122:125], v[142:145], v[166:169], v[122:125]
	v_mfma_f32_16x16x32_bf16 v[122:125], v[138:141], v[162:165], v[122:125]
	v_mfma_f32_16x16x32_bf16 v[106:109], v[138:141], v[170:173], v[106:109]
	v_mfma_f32_16x16x32_bf16 v[106:109], v[142:145], v[174:177], v[106:109]
	v_mfma_f32_16x16x32_bf16 v[114:117], v[134:137], v[174:177], v[114:117]
	v_mfma_f32_16x16x32_bf16 v[114:117], v[130:133], v[170:173], v[114:117]
	v_mfma_f32_16x16x32_bf16 v[102:105], v[130:133], v[178:181], v[102:105]
	v_mfma_f32_16x16x32_bf16 v[102:105], v[134:137], v[182:185], v[102:105]
	v_mfma_f32_16x16x32_bf16 v[94:97], v[142:145], v[182:185], v[94:97]
	v_mfma_f32_16x16x32_bf16 v[94:97], v[138:141], v[178:181], v[94:97]
	v_mfma_f32_16x16x32_bf16 v[78:81], v[138:141], v[186:189], v[78:81]
	v_mfma_f32_16x16x32_bf16 v[78:81], v[142:145], v[212:215], v[78:81]
	v_mfma_f32_16x16x32_bf16 v[86:89], v[134:137], v[212:215], v[86:89]
	v_mfma_f32_16x16x32_bf16 v[86:89], v[130:133], v[186:189], v[86:89]
	v_mfma_f32_16x16x32_bf16 v[118:121], v[146:149], v[162:165], v[118:121]
	v_mfma_f32_16x16x32_bf16 v[118:121], v[150:153], v[166:169], v[118:121]
	v_mfma_f32_16x16x32_bf16 v[110:113], v[158:161], v[166:169], v[110:113]
	v_mfma_f32_16x16x32_bf16 v[110:113], v[154:157], v[162:165], v[110:113]
	v_mfma_f32_16x16x32_bf16 v[90:93], v[154:157], v[170:173], v[90:93]
	v_mfma_f32_16x16x32_bf16 v[90:93], v[158:161], v[174:177], v[90:93]
	v_mfma_f32_16x16x32_bf16 v[98:101], v[150:153], v[174:177], v[98:101]
	v_mfma_f32_16x16x32_bf16 v[98:101], v[146:149], v[170:173], v[98:101]
	v_mfma_f32_16x16x32_bf16 v[82:85], v[146:149], v[178:181], v[82:85]
	v_mfma_f32_16x16x32_bf16 v[82:85], v[150:153], v[182:185], v[82:85]
	v_mfma_f32_16x16x32_bf16 v[74:77], v[158:161], v[182:185], v[74:77]
	v_mfma_f32_16x16x32_bf16 v[74:77], v[154:157], v[178:181], v[74:77]
	v_mfma_f32_16x16x32_bf16 v[66:69], v[154:157], v[186:189], v[66:69]
	v_mfma_f32_16x16x32_bf16 v[66:69], v[158:161], v[212:215], v[66:69]
	v_mfma_f32_16x16x32_bf16 v[70:73], v[150:153], v[212:215], v[70:73]
	v_mfma_f32_16x16x32_bf16 v[70:73], v[146:149], v[186:189], v[70:73]
	s_barrier
	s_mov_b32 m0, s79
	s_or_b32 s87, s86, 0x80
	ds_read_b128 v[162:165], v222 offset:49152
	ds_read_b128 v[166:169], v222 offset:50176
	ds_read_b128 v[170:173], v222 offset:51200
	ds_read_b128 v[174:177], v222 offset:52224
	ds_read_b128 v[178:181], v222 offset:53248
	ds_read_b128 v[182:185], v222 offset:54272
	ds_read_b128 v[186:189], v222 offset:55296
	ds_read_b128 v[212:215], v222 offset:56320
	buffer_load_dwordx4 v191, s[44:47], s87 offen lds
	s_mov_b32 m0, s80
	s_add_i32 s86, s86, 0x80080
	buffer_load_dwordx4 v217, s[44:47], s87 offen lds
	s_mov_b32 m0, s83
	s_nop 0
	buffer_load_dwordx4 v191, s[44:47], s86 offen lds
	s_mov_b32 m0, s92
	s_nop 0
	buffer_load_dwordx4 v217, s[44:47], s86 offen lds
	s_mov_b32 m0, s81
	s_nop 0
	buffer_load_dwordx4 v1, s[40:43], s85 offen lds
	s_mov_b32 m0, s82
	s_nop 0
	buffer_load_dwordx4 v216, s[40:43], s85 offen lds
	s_waitcnt vmcnt(8)
	s_waitcnt lgkmcnt(0)
	s_barrier
	v_mfma_f32_16x16x32_bf16 v[62:65], v[130:133], v[162:165], v[62:65]
	v_mfma_f32_16x16x32_bf16 v[62:65], v[134:137], v[166:169], v[62:65]
	v_mfma_f32_16x16x32_bf16 v[58:61], v[142:145], v[166:169], v[58:61]
	v_mfma_f32_16x16x32_bf16 v[58:61], v[138:141], v[162:165], v[58:61]
	v_mfma_f32_16x16x32_bf16 v[46:49], v[138:141], v[170:173], v[46:49]
	v_mfma_f32_16x16x32_bf16 v[46:49], v[142:145], v[174:177], v[46:49]
	v_mfma_f32_16x16x32_bf16 v[54:57], v[134:137], v[174:177], v[54:57]
	v_mfma_f32_16x16x32_bf16 v[54:57], v[130:133], v[170:173], v[54:57]
	v_mfma_f32_16x16x32_bf16 v[38:41], v[130:133], v[178:181], v[38:41]
	v_mfma_f32_16x16x32_bf16 v[38:41], v[134:137], v[182:185], v[38:41]
	v_mfma_f32_16x16x32_bf16 v[30:33], v[142:145], v[182:185], v[30:33]
	v_mfma_f32_16x16x32_bf16 v[30:33], v[138:141], v[178:181], v[30:33]
	v_mfma_f32_16x16x32_bf16 v[14:17], v[138:141], v[186:189], v[14:17]
	v_mfma_f32_16x16x32_bf16 v[14:17], v[142:145], v[212:215], v[14:17]
	v_mfma_f32_16x16x32_bf16 v[22:25], v[134:137], v[212:215], v[22:25]
	v_mfma_f32_16x16x32_bf16 v[22:25], v[130:133], v[186:189], v[22:25]
	v_mfma_f32_16x16x32_bf16 v[50:53], v[146:149], v[162:165], v[50:53]
	v_mfma_f32_16x16x32_bf16 v[50:53], v[150:153], v[166:169], v[50:53]
	v_mfma_f32_16x16x32_bf16 v[42:45], v[158:161], v[166:169], v[42:45]
	v_mfma_f32_16x16x32_bf16 v[42:45], v[154:157], v[162:165], v[42:45]
	v_mfma_f32_16x16x32_bf16 v[26:29], v[154:157], v[170:173], v[26:29]
	v_mfma_f32_16x16x32_bf16 v[26:29], v[158:161], v[174:177], v[26:29]
	v_mfma_f32_16x16x32_bf16 v[34:37], v[150:153], v[174:177], v[34:37]
	v_mfma_f32_16x16x32_bf16 v[34:37], v[146:149], v[170:173], v[34:37]
	v_mfma_f32_16x16x32_bf16 v[18:21], v[146:149], v[178:181], v[18:21]
	v_mfma_f32_16x16x32_bf16 v[18:21], v[150:153], v[182:185], v[18:21]
	v_mfma_f32_16x16x32_bf16 v[10:13], v[158:161], v[182:185], v[10:13]
	v_mfma_f32_16x16x32_bf16 v[10:13], v[154:157], v[178:181], v[10:13]
	v_mfma_f32_16x16x32_bf16 v[2:5], v[154:157], v[186:189], v[2:5]
	v_mfma_f32_16x16x32_bf16 v[2:5], v[158:161], v[212:215], v[2:5]
	v_mfma_f32_16x16x32_bf16 v[6:9], v[150:153], v[212:215], v[6:9]
	v_mfma_f32_16x16x32_bf16 v[6:9], v[146:149], v[186:189], v[6:9]
	s_barrier
	s_add_i32 s84, s84, 2
	s_addk_i32 s64, 0x100
	s_addk_i32 s65, 0x100
	s_cmp_gt_u32 s84, 29
	s_cbranch_scc0 .LBB0_114
	s_and_b64 vcc, exec, s[56:57]
	s_cbranch_vccz .LBB0_127
	s_barrier
	s_cmp_gt_i32 s61, 23
	s_mov_b64 s[46:47], -1
	s_cbranch_scc1 .LBB0_128

.LBB0_563:
	v_add_u32_e32 v3, 0x10000, v209
	ds_read_b128 v[140:143], v3
	ds_read_b128 v[144:147], v3 offset:1024
	ds_read_b128 v[148:151], v3 offset:2048
	ds_read_b128 v[152:155], v3 offset:3072
	v_add_u32_e32 v3, 0x14000, v209
	ds_read_b128 v[156:159], v3
	ds_read_b128 v[160:163], v3 offset:1024
	ds_read_b128 v[164:167], v3 offset:2048
	ds_read_b128 v[168:171], v3 offset:3072
	s_add_i32 s10, s57, 0xfff80080
	s_cmp_eq_u32 s59, 12
	s_cselect_b32 s62, s2, s10
	s_cselect_b32 s61, s3, s58
	s_add_i32 s60, s62, 0x80
	s_mov_b32 m0, s44
	ds_read_b128 v[172:175], v210
	ds_read_b128 v[176:179], v210 offset:1024
	ds_read_b128 v[180:183], v210 offset:2048
	ds_read_b128 v[184:187], v210 offset:3072
	ds_read_b128 v[188:191], v210 offset:4096
	ds_read_b128 v[192:195], v210 offset:5120
	ds_read_b128 v[196:199], v210 offset:6144
	ds_read_b128 v[200:203], v210 offset:7168
	buffer_load_dwordx4 v1, s[4:7], s57 offen lds
	s_mov_b32 m0, s45
	s_nop 0
	buffer_load_dwordx4 v206, s[4:7], s57 offen lds
	s_waitcnt vmcnt(8)
	s_waitcnt lgkmcnt(0)
	s_barrier
	v_mfma_f32_16x16x32_bf16 v[130:133], v[140:143], v[172:175], v[130:133]
	v_mfma_f32_16x16x32_bf16 v[130:133], v[144:147], v[176:179], v[130:133]
	v_mfma_f32_16x16x32_bf16 v[126:129], v[152:155], v[176:179], v[126:129]
	v_mfma_f32_16x16x32_bf16 v[126:129], v[148:151], v[172:175], v[126:129]
	v_mfma_f32_16x16x32_bf16 v[118:121], v[148:151], v[180:183], v[118:121]
	v_mfma_f32_16x16x32_bf16 v[118:121], v[152:155], v[184:187], v[118:121]
	v_mfma_f32_16x16x32_bf16 v[122:125], v[144:147], v[184:187], v[122:125]
	v_mfma_f32_16x16x32_bf16 v[122:125], v[140:143], v[180:183], v[122:125]
	v_mfma_f32_16x16x32_bf16 v[114:117], v[140:143], v[188:191], v[114:117]
	v_mfma_f32_16x16x32_bf16 v[114:117], v[144:147], v[192:195], v[114:117]
	v_mfma_f32_16x16x32_bf16 v[110:113], v[152:155], v[192:195], v[110:113]
	v_mfma_f32_16x16x32_bf16 v[110:113], v[148:151], v[188:191], v[110:113]
	v_mfma_f32_16x16x32_bf16 v[102:105], v[148:151], v[196:199], v[102:105]
	v_mfma_f32_16x16x32_bf16 v[102:105], v[152:155], v[200:203], v[102:105]
	v_mfma_f32_16x16x32_bf16 v[106:109], v[144:147], v[200:203], v[106:109]
	v_mfma_f32_16x16x32_bf16 v[106:109], v[140:143], v[196:199], v[106:109]
	v_mfma_f32_16x16x32_bf16 v[98:101], v[156:159], v[172:175], v[98:101]
	v_mfma_f32_16x16x32_bf16 v[98:101], v[160:163], v[176:179], v[98:101]
	v_mfma_f32_16x16x32_bf16 v[94:97], v[168:171], v[176:179], v[94:97]
	v_mfma_f32_16x16x32_bf16 v[94:97], v[164:167], v[172:175], v[94:97]
	v_mfma_f32_16x16x32_bf16 v[86:89], v[164:167], v[180:183], v[86:89]
	v_mfma_f32_16x16x32_bf16 v[86:89], v[168:171], v[184:187], v[86:89]
	v_mfma_f32_16x16x32_bf16 v[90:93], v[160:163], v[184:187], v[90:93]
	v_mfma_f32_16x16x32_bf16 v[90:93], v[156:159], v[180:183], v[90:93]
	v_mfma_f32_16x16x32_bf16 v[82:85], v[156:159], v[188:191], v[82:85]
	v_mfma_f32_16x16x32_bf16 v[82:85], v[160:163], v[192:195], v[82:85]
	v_mfma_f32_16x16x32_bf16 v[78:81], v[168:171], v[192:195], v[78:81]
	v_mfma_f32_16x16x32_bf16 v[78:81], v[164:167], v[188:191], v[78:81]
	v_mfma_f32_16x16x32_bf16 v[70:73], v[164:167], v[196:199], v[70:73]
	v_mfma_f32_16x16x32_bf16 v[70:73], v[168:171], v[200:203], v[70:73]
	v_mfma_f32_16x16x32_bf16 v[74:77], v[160:163], v[200:203], v[74:77]
	v_mfma_f32_16x16x32_bf16 v[74:77], v[156:159], v[196:199], v[74:77]
	s_barrier
	s_mov_b32 m0, s28
	s_mov_b32 s10, s6
	s_mov_b32 s11, s7
	ds_read_b128 v[172:175], v210 offset:16384
	ds_read_b128 v[176:179], v210 offset:17408
	ds_read_b128 v[180:183], v210 offset:18432
	ds_read_b128 v[184:187], v210 offset:19456
	ds_read_b128 v[188:191], v210 offset:20480
	ds_read_b128 v[192:195], v210 offset:21504
	ds_read_b128 v[196:199], v210 offset:22528
	ds_read_b128 v[200:203], v210 offset:23552
	buffer_load_dwordx4 v135, s[8:11], s61 offen lds
	s_mov_b32 m0, s29
	s_add_i32 s63, s61, 0x80000
	buffer_load_dwordx4 v207, s[8:11], s61 offen lds
	s_mov_b32 m0, s30
	s_nop 0
	buffer_load_dwordx4 v135, s[8:11], s63 offen lds
	s_mov_b32 m0, s31
	s_nop 0
	buffer_load_dwordx4 v207, s[8:11], s63 offen lds
	s_mov_b32 m0, s27
	s_nop 0
	buffer_load_dwordx4 v1, s[4:7], s62 offen lds
	s_mov_b32 m0, s33
	s_nop 0
	buffer_load_dwordx4 v206, s[4:7], s62 offen lds
	s_waitcnt vmcnt(8)
	s_waitcnt lgkmcnt(0)
	s_barrier
	v_mfma_f32_16x16x32_bf16 v[66:69], v[140:143], v[172:175], v[66:69]
	v_mfma_f32_16x16x32_bf16 v[66:69], v[144:147], v[176:179], v[66:69]
	v_mfma_f32_16x16x32_bf16 v[62:65], v[152:155], v[176:179], v[62:65]
	v_mfma_f32_16x16x32_bf16 v[62:65], v[148:151], v[172:175], v[62:65]
	v_mfma_f32_16x16x32_bf16 v[54:57], v[148:151], v[180:183], v[54:57]
	v_mfma_f32_16x16x32_bf16 v[54:57], v[152:155], v[184:187], v[54:57]
	v_mfma_f32_16x16x32_bf16 v[58:61], v[144:147], v[184:187], v[58:61]
	v_mfma_f32_16x16x32_bf16 v[58:61], v[140:143], v[180:183], v[58:61]
	v_mfma_f32_16x16x32_bf16 v[50:53], v[140:143], v[188:191], v[50:53]
	v_mfma_f32_16x16x32_bf16 v[50:53], v[144:147], v[192:195], v[50:53]
	v_mfma_f32_16x16x32_bf16 v[46:49], v[152:155], v[192:195], v[46:49]
	v_mfma_f32_16x16x32_bf16 v[46:49], v[148:151], v[188:191], v[46:49]
	v_mfma_f32_16x16x32_bf16 v[38:41], v[148:151], v[196:199], v[38:41]
	v_mfma_f32_16x16x32_bf16 v[38:41], v[152:155], v[200:203], v[38:41]
	v_mfma_f32_16x16x32_bf16 v[42:45], v[144:147], v[200:203], v[42:45]
	v_mfma_f32_16x16x32_bf16 v[42:45], v[140:143], v[196:199], v[42:45]
	v_mfma_f32_16x16x32_bf16 v[34:37], v[156:159], v[172:175], v[34:37]
	v_mfma_f32_16x16x32_bf16 v[34:37], v[160:163], v[176:179], v[34:37]
	v_mfma_f32_16x16x32_bf16 v[30:33], v[164:167], v[172:175], v[30:33]
	v_mfma_f32_16x16x32_bf16 v[30:33], v[168:171], v[176:179], v[30:33]
	v_mfma_f32_16x16x32_bf16 v[26:29], v[156:159], v[180:183], v[26:29]
	v_mfma_f32_16x16x32_bf16 v[26:29], v[160:163], v[184:187], v[26:29]
	v_mfma_f32_16x16x32_bf16 v[22:25], v[164:167], v[180:183], v[22:25]
	v_mfma_f32_16x16x32_bf16 v[22:25], v[168:171], v[184:187], v[22:25]
	v_mfma_f32_16x16x32_bf16 v[18:21], v[156:159], v[188:191], v[18:21]
	v_mfma_f32_16x16x32_bf16 v[18:21], v[160:163], v[192:195], v[18:21]
	v_mfma_f32_16x16x32_bf16 v[14:17], v[164:167], v[188:191], v[14:17]
	v_mfma_f32_16x16x32_bf16 v[14:17], v[168:171], v[192:195], v[14:17]
	v_mfma_f32_16x16x32_bf16 v[10:13], v[156:159], v[196:199], v[10:13]
	v_mfma_f32_16x16x32_bf16 v[10:13], v[160:163], v[200:203], v[10:13]
	v_mfma_f32_16x16x32_bf16 v[4:7], v[164:167], v[196:199], v[6:9]
	v_mfma_f32_16x16x32_bf16 v[4:7], v[168:171], v[200:203], v[4:7]
	s_barrier
	v_add_u32_e32 v3, 0x18000, v209
	ds_read_b128 v[140:143], v3
	ds_read_b128 v[144:147], v3 offset:1024
	ds_read_b128 v[148:151], v3 offset:2048
	ds_read_b128 v[152:155], v3 offset:3072
	v_add_u32_e32 v3, 0x1c000, v209
	ds_read_b128 v[156:159], v3
	ds_read_b128 v[160:163], v3 offset:1024
	ds_read_b128 v[164:167], v3 offset:2048
	ds_read_b128 v[168:171], v3 offset:3072
	s_add_i32 s62, s62, 0x80000
	s_mov_b32 m0, s34
	ds_read_b128 v[172:175], v210 offset:32768
	ds_read_b128 v[176:179], v210 offset:33792
	ds_read_b128 v[180:183], v210 offset:34816
	ds_read_b128 v[184:187], v210 offset:35840
	ds_read_b128 v[188:191], v210 offset:36864
	ds_read_b128 v[192:195], v210 offset:37888
	ds_read_b128 v[196:199], v210 offset:38912
	ds_read_b128 v[200:203], v210 offset:39936
	buffer_load_dwordx4 v1, s[4:7], s62 offen lds
	s_mov_b32 m0, s35
	s_nop 0
	buffer_load_dwordx4 v206, s[4:7], s62 offen lds
	s_waitcnt vmcnt(8)
	s_waitcnt lgkmcnt(0)
	s_nop 0
	s_barrier
	v_mfma_f32_16x16x32_bf16 v[130:133], v[140:143], v[172:175], v[130:133]
	v_mfma_f32_16x16x32_bf16 v[130:133], v[144:147], v[176:179], v[130:133]
	v_mfma_f32_16x16x32_bf16 v[126:129], v[152:155], v[176:179], v[126:129]
	v_mfma_f32_16x16x32_bf16 v[126:129], v[148:151], v[172:175], v[126:129]
	v_mfma_f32_16x16x32_bf16 v[118:121], v[148:151], v[180:183], v[118:121]
	v_mfma_f32_16x16x32_bf16 v[118:121], v[152:155], v[184:187], v[118:121]
	v_mfma_f32_16x16x32_bf16 v[122:125], v[144:147], v[184:187], v[122:125]
	v_mfma_f32_16x16x32_bf16 v[122:125], v[140:143], v[180:183], v[122:125]
	v_mfma_f32_16x16x32_bf16 v[114:117], v[140:143], v[188:191], v[114:117]
	v_mfma_f32_16x16x32_bf16 v[114:117], v[144:147], v[192:195], v[114:117]
	v_mfma_f32_16x16x32_bf16 v[110:113], v[152:155], v[192:195], v[110:113]
	v_mfma_f32_16x16x32_bf16 v[110:113], v[148:151], v[188:191], v[110:113]
	v_mfma_f32_16x16x32_bf16 v[102:105], v[148:151], v[196:199], v[102:105]
	v_mfma_f32_16x16x32_bf16 v[102:105], v[152:155], v[200:203], v[102:105]
	v_mfma_f32_16x16x32_bf16 v[106:109], v[144:147], v[200:203], v[106:109]
	v_mfma_f32_16x16x32_bf16 v[106:109], v[140:143], v[196:199], v[106:109]
	v_mfma_f32_16x16x32_bf16 v[98:101], v[156:159], v[172:175], v[98:101]
	v_mfma_f32_16x16x32_bf16 v[98:101], v[160:163], v[176:179], v[98:101]
	v_mfma_f32_16x16x32_bf16 v[94:97], v[168:171], v[176:179], v[94:97]
	v_mfma_f32_16x16x32_bf16 v[94:97], v[164:167], v[172:175], v[94:97]
	v_mfma_f32_16x16x32_bf16 v[86:89], v[164:167], v[180:183], v[86:89]
	v_mfma_f32_16x16x32_bf16 v[86:89], v[168:171], v[184:187], v[86:89]
	v_mfma_f32_16x16x32_bf16 v[90:93], v[160:163], v[184:187], v[90:93]
	v_mfma_f32_16x16x32_bf16 v[90:93], v[156:159], v[180:183], v[90:93]
	v_mfma_f32_16x16x32_bf16 v[82:85], v[156:159], v[188:191], v[82:85]
	v_mfma_f32_16x16x32_bf16 v[82:85], v[160:163], v[192:195], v[82:85]
	v_mfma_f32_16x16x32_bf16 v[78:81], v[168:171], v[192:195], v[78:81]
	v_mfma_f32_16x16x32_bf16 v[78:81], v[164:167], v[188:191], v[78:81]
	v_mfma_f32_16x16x32_bf16 v[70:73], v[164:167], v[196:199], v[70:73]
	v_mfma_f32_16x16x32_bf16 v[70:73], v[168:171], v[200:203], v[70:73]
	v_mfma_f32_16x16x32_bf16 v[74:77], v[160:163], v[200:203], v[74:77]
	v_mfma_f32_16x16x32_bf16 v[74:77], v[156:159], v[196:199], v[74:77]
	s_barrier
	s_mov_b32 m0, s38
	s_add_i32 s62, s61, 0x80
	ds_read_b128 v[172:175], v210 offset:49152
	ds_read_b128 v[176:179], v210 offset:50176
	ds_read_b128 v[180:183], v210 offset:51200
	ds_read_b128 v[184:187], v210 offset:52224
	ds_read_b128 v[188:191], v210 offset:53248
	ds_read_b128 v[192:195], v210 offset:54272
	ds_read_b128 v[196:199], v210 offset:55296
	ds_read_b128 v[200:203], v210 offset:56320
	buffer_load_dwordx4 v135, s[8:11], s62 offen lds
	s_mov_b32 m0, s39
	s_add_i32 s61, s61, 0x80080
	buffer_load_dwordx4 v207, s[8:11], s62 offen lds
	s_mov_b32 m0, s42
	s_nop 0
	buffer_load_dwordx4 v135, s[8:11], s61 offen lds
	s_mov_b32 m0, s43
	s_nop 0
	buffer_load_dwordx4 v207, s[8:11], s61 offen lds
	s_mov_b32 m0, s40
	s_nop 0
	buffer_load_dwordx4 v1, s[4:7], s60 offen lds
	s_mov_b32 m0, s41
	s_nop 0
	buffer_load_dwordx4 v206, s[4:7], s60 offen lds
	s_waitcnt vmcnt(8)
	s_waitcnt lgkmcnt(0)
	s_barrier
	v_mfma_f32_16x16x32_bf16 v[66:69], v[140:143], v[172:175], v[66:69]
	v_mfma_f32_16x16x32_bf16 v[66:69], v[144:147], v[176:179], v[66:69]
	v_mfma_f32_16x16x32_bf16 v[62:65], v[152:155], v[176:179], v[62:65]
	v_mfma_f32_16x16x32_bf16 v[62:65], v[148:151], v[172:175], v[62:65]
	v_mfma_f32_16x16x32_bf16 v[54:57], v[148:151], v[180:183], v[54:57]
	v_mfma_f32_16x16x32_bf16 v[54:57], v[152:155], v[184:187], v[54:57]
	v_mfma_f32_16x16x32_bf16 v[58:61], v[144:147], v[184:187], v[58:61]
	v_mfma_f32_16x16x32_bf16 v[58:61], v[140:143], v[180:183], v[58:61]
	v_mfma_f32_16x16x32_bf16 v[50:53], v[140:143], v[188:191], v[50:53]
	v_mfma_f32_16x16x32_bf16 v[50:53], v[144:147], v[192:195], v[50:53]
	v_mfma_f32_16x16x32_bf16 v[46:49], v[152:155], v[192:195], v[46:49]
	v_mfma_f32_16x16x32_bf16 v[46:49], v[148:151], v[188:191], v[46:49]
	v_mfma_f32_16x16x32_bf16 v[38:41], v[148:151], v[196:199], v[38:41]
	v_mfma_f32_16x16x32_bf16 v[38:41], v[152:155], v[200:203], v[38:41]
	v_mfma_f32_16x16x32_bf16 v[42:45], v[144:147], v[200:203], v[42:45]
	v_mfma_f32_16x16x32_bf16 v[42:45], v[140:143], v[196:199], v[42:45]
	v_mfma_f32_16x16x32_bf16 v[34:37], v[156:159], v[172:175], v[34:37]
	v_mfma_f32_16x16x32_bf16 v[34:37], v[160:163], v[176:179], v[34:37]
	v_mfma_f32_16x16x32_bf16 v[30:33], v[164:167], v[172:175], v[30:33]
	v_mfma_f32_16x16x32_bf16 v[30:33], v[168:171], v[176:179], v[30:33]
	v_mfma_f32_16x16x32_bf16 v[26:29], v[156:159], v[180:183], v[26:29]
	v_mfma_f32_16x16x32_bf16 v[26:29], v[160:163], v[184:187], v[26:29]
	v_mfma_f32_16x16x32_bf16 v[22:25], v[164:167], v[180:183], v[22:25]
	v_mfma_f32_16x16x32_bf16 v[22:25], v[168:171], v[184:187], v[22:25]
	v_mfma_f32_16x16x32_bf16 v[18:21], v[156:159], v[188:191], v[18:21]
	v_mfma_f32_16x16x32_bf16 v[18:21], v[160:163], v[192:195], v[18:21]
	v_mfma_f32_16x16x32_bf16 v[14:17], v[164:167], v[188:191], v[14:17]
	v_mfma_f32_16x16x32_bf16 v[14:17], v[168:171], v[192:195], v[14:17]
	v_mfma_f32_16x16x32_bf16 v[8:11], v[156:159], v[196:199], v[10:13]
	v_mfma_f32_16x16x32_bf16 v[10:13], v[160:163], v[200:203], v[8:11]
	v_mfma_f32_16x16x32_bf16 v[4:7], v[164:167], v[196:199], v[4:7]
	v_mfma_f32_16x16x32_bf16 v[6:9], v[168:171], v[200:203], v[4:7]
	s_barrier
	s_add_i32 s59, s59, 2
	s_addk_i32 s57, 0x100
	s_addk_i32 s58, 0x100
	s_cmp_gt_u32 s59, 13
	s_cbranch_scc0 .LBB0_563
	s_and_b64 vcc, exec, s[20:21]
	s_cbranch_vccz .LBB0_566
	s_barrier

.LBB0_686:
	v_add_u32_e32 v152, 0x10000, v138
	v_add_u32_e32 v168, 0x14000, v138
	ds_read_b128 v[140:143], v152
	ds_read_b128 v[144:147], v152 offset:1024
	ds_read_b128 v[148:151], v152 offset:2048
	ds_read_b128 v[152:155], v152 offset:3072
	ds_read_b128 v[156:159], v168
	ds_read_b128 v[160:163], v168 offset:1024
	ds_read_b128 v[164:167], v168 offset:2048
	ds_read_b128 v[168:171], v168 offset:3072
	s_add_i32 s10, s33, s52
	s_add_i32 s53, s27, s52
	s_add_i32 s11, s10, 0x1000
	s_addk_i32 s53, 0x1000
	s_cmp_eq_u32 s52, 0
	s_cselect_b32 s55, s49, s11
	s_cselect_b32 s54, s50, s53
	s_or_b32 s53, s55, 0x80
	s_add_i32 s10, s10, 0x80f80
	s_mov_b32 m0, s43
	ds_read_b128 v[172:175], v139
	ds_read_b128 v[176:179], v139 offset:1024
	ds_read_b128 v[180:183], v139 offset:2048
	ds_read_b128 v[184:187], v139 offset:3072
	ds_read_b128 v[188:191], v139 offset:4096
	ds_read_b128 v[192:195], v139 offset:5120
	ds_read_b128 v[196:199], v139 offset:6144
	ds_read_b128 v[200:203], v139 offset:7168
	buffer_load_dwordx4 v134, s[4:7], s10 offen lds
	s_mov_b32 m0, s44
	s_nop 0
	buffer_load_dwordx4 v136, s[4:7], s10 offen lds
	s_waitcnt vmcnt(8)
	s_waitcnt lgkmcnt(0)
	s_barrier
	v_mfma_f32_16x16x32_bf16 v[126:129], v[140:143], v[172:175], v[126:129]
	v_mfma_f32_16x16x32_bf16 v[126:129], v[144:147], v[176:179], v[126:129]
	v_mfma_f32_16x16x32_bf16 v[122:125], v[152:155], v[176:179], v[122:125]
	v_mfma_f32_16x16x32_bf16 v[122:125], v[148:151], v[172:175], v[122:125]
	v_mfma_f32_16x16x32_bf16 v[106:109], v[148:151], v[180:183], v[106:109]
	v_mfma_f32_16x16x32_bf16 v[106:109], v[152:155], v[184:187], v[106:109]
	v_mfma_f32_16x16x32_bf16 v[110:113], v[144:147], v[184:187], v[110:113]
	v_mfma_f32_16x16x32_bf16 v[110:113], v[140:143], v[180:183], v[110:113]
	v_mfma_f32_16x16x32_bf16 v[98:101], v[140:143], v[188:191], v[98:101]
	v_mfma_f32_16x16x32_bf16 v[98:101], v[144:147], v[192:195], v[98:101]
	v_mfma_f32_16x16x32_bf16 v[90:93], v[152:155], v[192:195], v[90:93]
	v_mfma_f32_16x16x32_bf16 v[90:93], v[148:151], v[188:191], v[90:93]
	v_mfma_f32_16x16x32_bf16 v[74:77], v[148:151], v[196:199], v[74:77]
	v_mfma_f32_16x16x32_bf16 v[74:77], v[152:155], v[200:203], v[74:77]
	v_mfma_f32_16x16x32_bf16 v[82:85], v[144:147], v[200:203], v[82:85]
	v_mfma_f32_16x16x32_bf16 v[82:85], v[140:143], v[196:199], v[82:85]
	v_mfma_f32_16x16x32_bf16 v[118:121], v[156:159], v[172:175], v[118:121]
	v_mfma_f32_16x16x32_bf16 v[118:121], v[160:163], v[176:179], v[118:121]
	v_mfma_f32_16x16x32_bf16 v[114:117], v[168:171], v[176:179], v[114:117]
	v_mfma_f32_16x16x32_bf16 v[114:117], v[164:167], v[172:175], v[114:117]
	v_mfma_f32_16x16x32_bf16 v[94:97], v[164:167], v[180:183], v[94:97]
	v_mfma_f32_16x16x32_bf16 v[94:97], v[168:171], v[184:187], v[94:97]
	v_mfma_f32_16x16x32_bf16 v[102:105], v[160:163], v[184:187], v[102:105]
	v_mfma_f32_16x16x32_bf16 v[102:105], v[156:159], v[180:183], v[102:105]
	v_mfma_f32_16x16x32_bf16 v[86:89], v[156:159], v[188:191], v[86:89]
	v_mfma_f32_16x16x32_bf16 v[86:89], v[160:163], v[192:195], v[86:89]
	v_mfma_f32_16x16x32_bf16 v[78:81], v[168:171], v[192:195], v[78:81]
	v_mfma_f32_16x16x32_bf16 v[78:81], v[164:167], v[188:191], v[78:81]
	v_mfma_f32_16x16x32_bf16 v[66:69], v[164:167], v[196:199], v[66:69]
	v_mfma_f32_16x16x32_bf16 v[66:69], v[168:171], v[200:203], v[66:69]
	v_mfma_f32_16x16x32_bf16 v[70:73], v[160:163], v[200:203], v[70:73]
	v_mfma_f32_16x16x32_bf16 v[70:73], v[156:159], v[196:199], v[70:73]
	s_barrier
	s_mov_b32 m0, s26
	s_mov_b32 s10, s6
	s_mov_b32 s11, s7
	ds_read_b128 v[172:175], v139 offset:16384
	ds_read_b128 v[176:179], v139 offset:17408
	ds_read_b128 v[180:183], v139 offset:18432
	ds_read_b128 v[184:187], v139 offset:19456
	ds_read_b128 v[188:191], v139 offset:20480
	ds_read_b128 v[192:195], v139 offset:21504
	ds_read_b128 v[196:199], v139 offset:22528
	ds_read_b128 v[200:203], v139 offset:23552
	buffer_load_dwordx4 v135, s[8:11], s54 offen lds
	s_mov_b32 m0, s28
	s_add_i32 s56, s54, 0x80000
	buffer_load_dwordx4 v137, s[8:11], s54 offen lds
	s_mov_b32 m0, s29
	s_nop 0
	buffer_load_dwordx4 v135, s[8:11], s56 offen lds
	s_mov_b32 m0, s30
	s_nop 0
	buffer_load_dwordx4 v137, s[8:11], s56 offen lds
	s_mov_b32 m0, s25
	s_nop 0
	buffer_load_dwordx4 v134, s[4:7], s55 offen lds
	s_mov_b32 m0, s31
	s_nop 0
	buffer_load_dwordx4 v136, s[4:7], s55 offen lds
	s_waitcnt vmcnt(8)
	s_waitcnt lgkmcnt(0)
	s_barrier
	v_mfma_f32_16x16x32_bf16 v[62:65], v[140:143], v[172:175], v[62:65]
	v_mfma_f32_16x16x32_bf16 v[62:65], v[144:147], v[176:179], v[62:65]
	v_mfma_f32_16x16x32_bf16 v[58:61], v[152:155], v[176:179], v[58:61]
	v_mfma_f32_16x16x32_bf16 v[58:61], v[148:151], v[172:175], v[58:61]
	v_mfma_f32_16x16x32_bf16 v[42:45], v[148:151], v[180:183], v[42:45]
	v_mfma_f32_16x16x32_bf16 v[42:45], v[152:155], v[184:187], v[42:45]
	v_mfma_f32_16x16x32_bf16 v[46:49], v[144:147], v[184:187], v[46:49]
	v_mfma_f32_16x16x32_bf16 v[46:49], v[140:143], v[180:183], v[46:49]
	v_mfma_f32_16x16x32_bf16 v[30:33], v[140:143], v[188:191], v[30:33]
	v_mfma_f32_16x16x32_bf16 v[30:33], v[144:147], v[192:195], v[30:33]
	v_mfma_f32_16x16x32_bf16 v[26:29], v[152:155], v[192:195], v[26:29]
	v_mfma_f32_16x16x32_bf16 v[26:29], v[148:151], v[188:191], v[26:29]
	v_mfma_f32_16x16x32_bf16 v[10:13], v[148:151], v[196:199], v[10:13]
	v_mfma_f32_16x16x32_bf16 v[10:13], v[152:155], v[200:203], v[10:13]
	v_mfma_f32_16x16x32_bf16 v[14:17], v[144:147], v[200:203], v[14:17]
	v_mfma_f32_16x16x32_bf16 v[14:17], v[140:143], v[196:199], v[14:17]
	v_mfma_f32_16x16x32_bf16 v[54:57], v[156:159], v[172:175], v[54:57]
	v_mfma_f32_16x16x32_bf16 v[54:57], v[160:163], v[176:179], v[54:57]
	v_mfma_f32_16x16x32_bf16 v[50:53], v[168:171], v[176:179], v[50:53]
	v_mfma_f32_16x16x32_bf16 v[50:53], v[164:167], v[172:175], v[50:53]
	v_mfma_f32_16x16x32_bf16 v[34:37], v[164:167], v[180:183], v[34:37]
	v_mfma_f32_16x16x32_bf16 v[34:37], v[168:171], v[184:187], v[34:37]
	v_mfma_f32_16x16x32_bf16 v[38:41], v[160:163], v[184:187], v[38:41]
	v_mfma_f32_16x16x32_bf16 v[38:41], v[156:159], v[180:183], v[38:41]
	v_mfma_f32_16x16x32_bf16 v[22:25], v[156:159], v[188:191], v[22:25]
	v_mfma_f32_16x16x32_bf16 v[22:25], v[160:163], v[192:195], v[22:25]
	v_mfma_f32_16x16x32_bf16 v[18:21], v[168:171], v[192:195], v[18:21]
	v_mfma_f32_16x16x32_bf16 v[18:21], v[164:167], v[188:191], v[18:21]
	v_mfma_f32_16x16x32_bf16 v[2:5], v[164:167], v[196:199], v[2:5]
	v_mfma_f32_16x16x32_bf16 v[2:5], v[168:171], v[200:203], v[2:5]
	v_mfma_f32_16x16x32_bf16 v[6:9], v[160:163], v[200:203], v[6:9]
	v_mfma_f32_16x16x32_bf16 v[6:9], v[156:159], v[196:199], v[6:9]
	s_barrier
	v_add_u32_e32 v152, 0x18000, v138
	v_add_u32_e32 v168, 0x1c000, v138
	ds_read_b128 v[140:143], v152
	ds_read_b128 v[144:147], v152 offset:1024
	ds_read_b128 v[148:151], v152 offset:2048
	ds_read_b128 v[152:155], v152 offset:3072
	ds_read_b128 v[156:159], v168
	ds_read_b128 v[160:163], v168 offset:1024
	ds_read_b128 v[164:167], v168 offset:2048
	ds_read_b128 v[168:171], v168 offset:3072
	s_add_i32 s55, s55, 0x80000
	s_mov_b32 m0, s34
	ds_read_b128 v[172:175], v139 offset:32768
	ds_read_b128 v[176:179], v139 offset:33792
	ds_read_b128 v[180:183], v139 offset:34816
	ds_read_b128 v[184:187], v139 offset:35840
	ds_read_b128 v[188:191], v139 offset:36864
	ds_read_b128 v[192:195], v139 offset:37888
	ds_read_b128 v[196:199], v139 offset:38912
	ds_read_b128 v[200:203], v139 offset:39936
	buffer_load_dwordx4 v134, s[4:7], s55 offen lds
	s_mov_b32 m0, s35
	s_nop 0
	buffer_load_dwordx4 v136, s[4:7], s55 offen lds
	s_waitcnt vmcnt(8)
	s_waitcnt lgkmcnt(0)
	s_nop 0
	s_barrier
	v_mfma_f32_16x16x32_bf16 v[126:129], v[140:143], v[172:175], v[126:129]
	v_mfma_f32_16x16x32_bf16 v[126:129], v[144:147], v[176:179], v[126:129]
	v_mfma_f32_16x16x32_bf16 v[122:125], v[152:155], v[176:179], v[122:125]
	v_mfma_f32_16x16x32_bf16 v[122:125], v[148:151], v[172:175], v[122:125]
	v_mfma_f32_16x16x32_bf16 v[106:109], v[148:151], v[180:183], v[106:109]
	v_mfma_f32_16x16x32_bf16 v[106:109], v[152:155], v[184:187], v[106:109]
	v_mfma_f32_16x16x32_bf16 v[110:113], v[144:147], v[184:187], v[110:113]
	v_mfma_f32_16x16x32_bf16 v[110:113], v[140:143], v[180:183], v[110:113]
	v_mfma_f32_16x16x32_bf16 v[98:101], v[140:143], v[188:191], v[98:101]
	v_mfma_f32_16x16x32_bf16 v[98:101], v[144:147], v[192:195], v[98:101]
	v_mfma_f32_16x16x32_bf16 v[90:93], v[152:155], v[192:195], v[90:93]
	v_mfma_f32_16x16x32_bf16 v[90:93], v[148:151], v[188:191], v[90:93]
	v_mfma_f32_16x16x32_bf16 v[74:77], v[148:151], v[196:199], v[74:77]
	v_mfma_f32_16x16x32_bf16 v[74:77], v[152:155], v[200:203], v[74:77]
	v_mfma_f32_16x16x32_bf16 v[82:85], v[144:147], v[200:203], v[82:85]
	v_mfma_f32_16x16x32_bf16 v[82:85], v[140:143], v[196:199], v[82:85]
	v_mfma_f32_16x16x32_bf16 v[118:121], v[156:159], v[172:175], v[118:121]
	v_mfma_f32_16x16x32_bf16 v[118:121], v[160:163], v[176:179], v[118:121]
	v_mfma_f32_16x16x32_bf16 v[114:117], v[168:171], v[176:179], v[114:117]
	v_mfma_f32_16x16x32_bf16 v[114:117], v[164:167], v[172:175], v[114:117]
	v_mfma_f32_16x16x32_bf16 v[94:97], v[164:167], v[180:183], v[94:97]
	v_mfma_f32_16x16x32_bf16 v[94:97], v[168:171], v[184:187], v[94:97]
	v_mfma_f32_16x16x32_bf16 v[102:105], v[160:163], v[184:187], v[102:105]
	v_mfma_f32_16x16x32_bf16 v[102:105], v[156:159], v[180:183], v[102:105]
	v_mfma_f32_16x16x32_bf16 v[86:89], v[156:159], v[188:191], v[86:89]
	v_mfma_f32_16x16x32_bf16 v[86:89], v[160:163], v[192:195], v[86:89]
	v_mfma_f32_16x16x32_bf16 v[78:81], v[168:171], v[192:195], v[78:81]
	v_mfma_f32_16x16x32_bf16 v[78:81], v[164:167], v[188:191], v[78:81]
	v_mfma_f32_16x16x32_bf16 v[66:69], v[164:167], v[196:199], v[66:69]
	v_mfma_f32_16x16x32_bf16 v[66:69], v[168:171], v[200:203], v[66:69]
	v_mfma_f32_16x16x32_bf16 v[70:73], v[160:163], v[200:203], v[70:73]
	v_mfma_f32_16x16x32_bf16 v[70:73], v[156:159], v[196:199], v[70:73]
	s_barrier
	s_mov_b32 m0, s36
	s_or_b32 s55, s54, 0x80
	ds_read_b128 v[172:175], v139 offset:49152
	ds_read_b128 v[176:179], v139 offset:50176
	ds_read_b128 v[180:183], v139 offset:51200
	ds_read_b128 v[184:187], v139 offset:52224
	ds_read_b128 v[188:191], v139 offset:53248
	ds_read_b128 v[192:195], v139 offset:54272
	ds_read_b128 v[196:199], v139 offset:55296
	ds_read_b128 v[200:203], v139 offset:56320
	buffer_load_dwordx4 v135, s[8:11], s55 offen lds
	s_mov_b32 m0, s37
	s_add_i32 s54, s54, 0x80080
	buffer_load_dwordx4 v137, s[8:11], s55 offen lds
	s_mov_b32 m0, s41
	s_nop 0
	buffer_load_dwordx4 v135, s[8:11], s54 offen lds
	s_mov_b32 m0, s42
	s_nop 0
	buffer_load_dwordx4 v137, s[8:11], s54 offen lds
	s_mov_b32 m0, s38
	s_nop 0
	buffer_load_dwordx4 v134, s[4:7], s53 offen lds
	s_mov_b32 m0, s40
	s_nop 0
	buffer_load_dwordx4 v136, s[4:7], s53 offen lds
	s_waitcnt vmcnt(8)
	s_waitcnt lgkmcnt(0)
	s_barrier
	v_mfma_f32_16x16x32_bf16 v[62:65], v[140:143], v[172:175], v[62:65]
	v_mfma_f32_16x16x32_bf16 v[62:65], v[144:147], v[176:179], v[62:65]
	v_mfma_f32_16x16x32_bf16 v[58:61], v[152:155], v[176:179], v[58:61]
	v_mfma_f32_16x16x32_bf16 v[58:61], v[148:151], v[172:175], v[58:61]
	v_mfma_f32_16x16x32_bf16 v[42:45], v[148:151], v[180:183], v[42:45]
	v_mfma_f32_16x16x32_bf16 v[42:45], v[152:155], v[184:187], v[42:45]
	v_mfma_f32_16x16x32_bf16 v[46:49], v[144:147], v[184:187], v[46:49]
	v_mfma_f32_16x16x32_bf16 v[46:49], v[140:143], v[180:183], v[46:49]
	v_mfma_f32_16x16x32_bf16 v[30:33], v[140:143], v[188:191], v[30:33]
	v_mfma_f32_16x16x32_bf16 v[30:33], v[144:147], v[192:195], v[30:33]
	v_mfma_f32_16x16x32_bf16 v[26:29], v[152:155], v[192:195], v[26:29]
	v_mfma_f32_16x16x32_bf16 v[26:29], v[148:151], v[188:191], v[26:29]
	v_mfma_f32_16x16x32_bf16 v[10:13], v[148:151], v[196:199], v[10:13]
	v_mfma_f32_16x16x32_bf16 v[10:13], v[152:155], v[200:203], v[10:13]
	v_mfma_f32_16x16x32_bf16 v[14:17], v[144:147], v[200:203], v[14:17]
	v_mfma_f32_16x16x32_bf16 v[14:17], v[140:143], v[196:199], v[14:17]
	v_mfma_f32_16x16x32_bf16 v[54:57], v[156:159], v[172:175], v[54:57]
	v_mfma_f32_16x16x32_bf16 v[54:57], v[160:163], v[176:179], v[54:57]
	v_mfma_f32_16x16x32_bf16 v[50:53], v[168:171], v[176:179], v[50:53]
	v_mfma_f32_16x16x32_bf16 v[50:53], v[164:167], v[172:175], v[50:53]
	v_mfma_f32_16x16x32_bf16 v[34:37], v[164:167], v[180:183], v[34:37]
	v_mfma_f32_16x16x32_bf16 v[34:37], v[168:171], v[184:187], v[34:37]
	v_mfma_f32_16x16x32_bf16 v[38:41], v[160:163], v[184:187], v[38:41]
	v_mfma_f32_16x16x32_bf16 v[38:41], v[156:159], v[180:183], v[38:41]
	v_mfma_f32_16x16x32_bf16 v[22:25], v[156:159], v[188:191], v[22:25]
	v_mfma_f32_16x16x32_bf16 v[22:25], v[160:163], v[192:195], v[22:25]
	v_mfma_f32_16x16x32_bf16 v[18:21], v[168:171], v[192:195], v[18:21]
	v_mfma_f32_16x16x32_bf16 v[18:21], v[164:167], v[188:191], v[18:21]
	v_mfma_f32_16x16x32_bf16 v[2:5], v[164:167], v[196:199], v[2:5]
	v_mfma_f32_16x16x32_bf16 v[2:5], v[168:171], v[200:203], v[2:5]
	v_mfma_f32_16x16x32_bf16 v[6:9], v[160:163], v[200:203], v[6:9]
	v_mfma_f32_16x16x32_bf16 v[6:9], v[156:159], v[196:199], v[6:9]
	s_barrier
	s_add_i32 s51, s51, 2
	s_addk_i32 s52, 0x100
	s_cmp_gt_u32 s51, 29
	s_cbranch_scc0 .LBB0_686
	s_andn2_b64 vcc, exec, s[2:3]
	s_cbranch_vccnz .LBB0_678
	v_mov_b32_e32 v2, 0
	s_mov_b32 s14, s46
	s_mov_b32 s15, s47
	s_mov_b32 s27, s48
	s_mov_b32 s33, s13
	s_mov_b32 s45, s12
	v_mov_b32_e32 v3, v2
	v_mov_b32_e32 v4, v2
	v_mov_b32_e32 v5, v2
	v_mov_b32_e32 v6, v2
	v_mov_b32_e32 v7, v2
	v_mov_b32_e32 v8, v2
	v_mov_b32_e32 v9, v2
	v_mov_b32_e32 v18, v2
	v_mov_b32_e32 v19, v2
	v_mov_b32_e32 v20, v2
	v_mov_b32_e32 v21, v2
	v_mov_b32_e32 v22, v2
	v_mov_b32_e32 v23, v2
	v_mov_b32_e32 v24, v2
	v_mov_b32_e32 v25, v2
	v_mov_b32_e32 v34, v2
	v_mov_b32_e32 v35, v2
	v_mov_b32_e32 v36, v2
	v_mov_b32_e32 v37, v2
	v_mov_b32_e32 v38, v2
	v_mov_b32_e32 v39, v2
	v_mov_b32_e32 v40, v2
	v_mov_b32_e32 v41, v2
	v_mov_b32_e32 v50, v2
	v_mov_b32_e32 v51, v2
	v_mov_b32_e32 v52, v2
	v_mov_b32_e32 v53, v2
	v_mov_b32_e32 v54, v2
	v_mov_b32_e32 v55, v2
	v_mov_b32_e32 v56, v2
	v_mov_b32_e32 v57, v2
	v_mov_b32_e32 v10, v2
	v_mov_b32_e32 v11, v2
	v_mov_b32_e32 v12, v2
	v_mov_b32_e32 v13, v2
	v_mov_b32_e32 v14, v2
	v_mov_b32_e32 v15, v2
	v_mov_b32_e32 v16, v2
	v_mov_b32_e32 v17, v2
	v_mov_b32_e32 v26, v2
	v_mov_b32_e32 v27, v2
	v_mov_b32_e32 v28, v2
	v_mov_b32_e32 v29, v2
	v_mov_b32_e32 v30, v2
	v_mov_b32_e32 v31, v2
	v_mov_b32_e32 v32, v2
	v_mov_b32_e32 v33, v2
	v_mov_b32_e32 v42, v2
	v_mov_b32_e32 v43, v2
	v_mov_b32_e32 v44, v2
	v_mov_b32_e32 v45, v2
	v_mov_b32_e32 v46, v2
	v_mov_b32_e32 v47, v2
	v_mov_b32_e32 v48, v2
	v_mov_b32_e32 v49, v2
	v_mov_b32_e32 v58, v2
	v_mov_b32_e32 v59, v2
	v_mov_b32_e32 v60, v2
	v_mov_b32_e32 v61, v2
	v_mov_b32_e32 v62, v2
	v_mov_b32_e32 v63, v2
	v_mov_b32_e32 v64, v2
	v_mov_b32_e32 v65, v2
	v_mov_b32_e32 v66, v2
	v_mov_b32_e32 v67, v2
	v_mov_b32_e32 v68, v2
	v_mov_b32_e32 v69, v2
	v_mov_b32_e32 v70, v2
	v_mov_b32_e32 v71, v2
	v_mov_b32_e32 v72, v2
	v_mov_b32_e32 v73, v2
	v_mov_b32_e32 v78, v2
	v_mov_b32_e32 v79, v2
	v_mov_b32_e32 v80, v2
	v_mov_b32_e32 v81, v2
	v_mov_b32_e32 v86, v2
	v_mov_b32_e32 v87, v2
	v_mov_b32_e32 v88, v2
	v_mov_b32_e32 v89, v2
	v_mov_b32_e32 v94, v2
	v_mov_b32_e32 v95, v2
	v_mov_b32_e32 v96, v2
	v_mov_b32_e32 v97, v2
	v_mov_b32_e32 v102, v2
	v_mov_b32_e32 v103, v2
	v_mov_b32_e32 v104, v2
	v_mov_b32_e32 v105, v2
	v_mov_b32_e32 v114, v2
	v_mov_b32_e32 v115, v2
	v_mov_b32_e32 v116, v2
	v_mov_b32_e32 v117, v2
	v_mov_b32_e32 v118, v2
	v_mov_b32_e32 v119, v2
	v_mov_b32_e32 v120, v2
	v_mov_b32_e32 v121, v2
	v_mov_b32_e32 v74, v2
	v_mov_b32_e32 v75, v2
	v_mov_b32_e32 v76, v2
	v_mov_b32_e32 v77, v2
	v_mov_b32_e32 v82, v2
	v_mov_b32_e32 v83, v2
	v_mov_b32_e32 v84, v2
	v_mov_b32_e32 v85, v2
	v_mov_b32_e32 v90, v2
	v_mov_b32_e32 v91, v2
	v_mov_b32_e32 v92, v2
	v_mov_b32_e32 v93, v2
	v_mov_b32_e32 v98, v2
	v_mov_b32_e32 v99, v2
	v_mov_b32_e32 v100, v2
	v_mov_b32_e32 v101, v2
	v_mov_b32_e32 v106, v2
	v_mov_b32_e32 v107, v2
	v_mov_b32_e32 v108, v2
	v_mov_b32_e32 v109, v2
	v_mov_b32_e32 v110, v2
	v_mov_b32_e32 v111, v2
	v_mov_b32_e32 v112, v2
	v_mov_b32_e32 v113, v2
	v_mov_b32_e32 v122, v2
	v_mov_b32_e32 v123, v2
	v_mov_b32_e32 v124, v2
	v_mov_b32_e32 v125, v2
	v_mov_b32_e32 v126, v2
	v_mov_b32_e32 v127, v2
	v_mov_b32_e32 v128, v2
	v_mov_b32_e32 v129, v2
	s_branch .LBB0_678

.LBB0_907:
	v_add_u32_e32 v166, 0x10000, v179
	ds_read_b128 v[162:165], v166
	ds_read_b128 v[182:185], v166 offset:1024
	ds_read_b128 v[186:189], v166 offset:2048
	ds_read_b128 v[190:193], v166 offset:3072
	v_add_u32_e32 v166, 0x14000, v179
	ds_read_b128 v[194:197], v166
	ds_read_b128 v[198:201], v166 offset:1024
	ds_read_b128 v[202:205], v166 offset:2048
	ds_read_b128 v[206:209], v166 offset:3072
	s_add_i32 s10, s45, s64
	s_add_i32 s26, s40, s64
	s_add_i32 s11, s10, 0x1000
	s_addk_i32 s26, 0x1000
	s_cmp_eq_u32 s64, 0
	s_cselect_b32 s29, s62, s11
	s_cselect_b32 s27, s63, s26
	s_add_i32 s26, s29, 0x80
	s_add_i32 s28, s27, 0x80
	s_add_i32 s10, s10, 0x80f80
	s_mov_b32 m0, s55
	ds_read_b128 v[210:213], v180
	ds_read_b128 v[214:217], v180 offset:1024
	ds_read_b128 v[218:221], v180 offset:2048
	ds_read_b128 v[222:225], v180 offset:3072
	ds_read_b128 v[226:229], v180 offset:4096
	ds_read_b128 v[230:233], v180 offset:5120
	ds_read_b128 v[234:237], v180 offset:6144
	ds_read_b128 v[238:241], v180 offset:7168
	buffer_load_dwordx4 v1, s[4:7], s10 offen lds
	s_mov_b32 m0, s56
	s_nop 0
	buffer_load_dwordx4 v175, s[4:7], s10 offen lds
	s_waitcnt vmcnt(8)
	s_waitcnt lgkmcnt(0)
	s_nop 0
	s_barrier
	v_mfma_f32_16x16x32_bf16 v[126:129], v[162:165], v[210:213], v[126:129]
	v_mfma_f32_16x16x32_bf16 v[126:129], v[182:185], v[214:217], v[126:129]
	v_mfma_f32_16x16x32_bf16 v[122:125], v[190:193], v[214:217], v[122:125]
	v_mfma_f32_16x16x32_bf16 v[122:125], v[186:189], v[210:213], v[122:125]
	v_mfma_f32_16x16x32_bf16 v[114:117], v[186:189], v[218:221], v[114:117]
	v_mfma_f32_16x16x32_bf16 v[114:117], v[190:193], v[222:225], v[114:117]
	v_mfma_f32_16x16x32_bf16 v[118:121], v[182:185], v[222:225], v[118:121]
	v_mfma_f32_16x16x32_bf16 v[118:121], v[162:165], v[218:221], v[118:121]
	v_mfma_f32_16x16x32_bf16 v[110:113], v[162:165], v[226:229], v[110:113]
	v_mfma_f32_16x16x32_bf16 v[110:113], v[182:185], v[230:233], v[110:113]
	v_mfma_f32_16x16x32_bf16 v[106:109], v[190:193], v[230:233], v[106:109]
	v_mfma_f32_16x16x32_bf16 v[106:109], v[186:189], v[226:229], v[106:109]
	v_mfma_f32_16x16x32_bf16 v[98:101], v[186:189], v[234:237], v[98:101]
	v_mfma_f32_16x16x32_bf16 v[98:101], v[190:193], v[238:241], v[98:101]
	v_mfma_f32_16x16x32_bf16 v[102:105], v[182:185], v[238:241], v[102:105]
	v_mfma_f32_16x16x32_bf16 v[102:105], v[162:165], v[234:237], v[102:105]
	v_mfma_f32_16x16x32_bf16 v[94:97], v[194:197], v[210:213], v[94:97]
	v_mfma_f32_16x16x32_bf16 v[94:97], v[198:201], v[214:217], v[94:97]
	v_mfma_f32_16x16x32_bf16 v[90:93], v[206:209], v[214:217], v[90:93]
	v_mfma_f32_16x16x32_bf16 v[90:93], v[202:205], v[210:213], v[90:93]
	v_mfma_f32_16x16x32_bf16 v[82:85], v[202:205], v[218:221], v[82:85]
	v_mfma_f32_16x16x32_bf16 v[82:85], v[206:209], v[222:225], v[82:85]
	v_mfma_f32_16x16x32_bf16 v[86:89], v[198:201], v[222:225], v[86:89]
	v_mfma_f32_16x16x32_bf16 v[86:89], v[194:197], v[218:221], v[86:89]
	v_mfma_f32_16x16x32_bf16 v[78:81], v[194:197], v[226:229], v[78:81]
	v_mfma_f32_16x16x32_bf16 v[78:81], v[198:201], v[230:233], v[78:81]
	v_mfma_f32_16x16x32_bf16 v[74:77], v[206:209], v[230:233], v[74:77]
	v_mfma_f32_16x16x32_bf16 v[74:77], v[202:205], v[226:229], v[74:77]
	v_mfma_f32_16x16x32_bf16 v[66:69], v[202:205], v[234:237], v[66:69]
	v_mfma_f32_16x16x32_bf16 v[66:69], v[206:209], v[238:241], v[66:69]
	v_mfma_f32_16x16x32_bf16 v[70:73], v[198:201], v[238:241], v[70:73]
	v_mfma_f32_16x16x32_bf16 v[70:73], v[194:197], v[234:237], v[70:73]
	s_barrier
	s_mov_b32 m0, s37
	s_mov_b32 s10, s6
	s_mov_b32 s11, s7
	ds_read_b128 v[210:213], v180 offset:16384
	ds_read_b128 v[214:217], v180 offset:17408
	ds_read_b128 v[218:221], v180 offset:18432
	ds_read_b128 v[222:225], v180 offset:19456
	ds_read_b128 v[226:229], v180 offset:20480
	ds_read_b128 v[230:233], v180 offset:21504
	ds_read_b128 v[234:237], v180 offset:22528
	ds_read_b128 v[238:241], v180 offset:23552
	buffer_load_dwordx4 v174, s[8:11], s27 offen lds
	s_mov_b32 m0, s38
	s_add_i32 s66, s27, 0x80000
	buffer_load_dwordx4 v176, s[8:11], s27 offen lds
	s_mov_b32 m0, s39
	s_nop 0
	buffer_load_dwordx4 v174, s[8:11], s66 offen lds
	s_mov_b32 m0, s41
	s_nop 0
	buffer_load_dwordx4 v176, s[8:11], s66 offen lds
	s_mov_b32 m0, s36
	s_nop 0
	buffer_load_dwordx4 v1, s[4:7], s29 offen lds
	s_mov_b32 m0, s42
	s_nop 0
	buffer_load_dwordx4 v175, s[4:7], s29 offen lds
	s_waitcnt vmcnt(8)
	s_waitcnt lgkmcnt(0)
	s_barrier
	v_mfma_f32_16x16x32_bf16 v[62:65], v[162:165], v[210:213], v[62:65]
	v_mfma_f32_16x16x32_bf16 v[62:65], v[182:185], v[214:217], v[62:65]
	v_mfma_f32_16x16x32_bf16 v[58:61], v[190:193], v[214:217], v[58:61]
	v_mfma_f32_16x16x32_bf16 v[58:61], v[186:189], v[210:213], v[58:61]
	v_mfma_f32_16x16x32_bf16 v[50:53], v[186:189], v[218:221], v[50:53]
	v_mfma_f32_16x16x32_bf16 v[50:53], v[190:193], v[222:225], v[50:53]
	v_mfma_f32_16x16x32_bf16 v[54:57], v[182:185], v[222:225], v[54:57]
	v_mfma_f32_16x16x32_bf16 v[54:57], v[162:165], v[218:221], v[54:57]
	v_mfma_f32_16x16x32_bf16 v[46:49], v[162:165], v[226:229], v[46:49]
	v_mfma_f32_16x16x32_bf16 v[46:49], v[182:185], v[230:233], v[46:49]
	v_mfma_f32_16x16x32_bf16 v[42:45], v[190:193], v[230:233], v[42:45]
	v_mfma_f32_16x16x32_bf16 v[42:45], v[186:189], v[226:229], v[42:45]
	v_mfma_f32_16x16x32_bf16 v[34:37], v[186:189], v[234:237], v[34:37]
	v_mfma_f32_16x16x32_bf16 v[34:37], v[190:193], v[238:241], v[34:37]
	v_mfma_f32_16x16x32_bf16 v[38:41], v[182:185], v[238:241], v[38:41]
	v_mfma_f32_16x16x32_bf16 v[38:41], v[162:165], v[234:237], v[38:41]
	v_mfma_f32_16x16x32_bf16 v[30:33], v[194:197], v[210:213], v[30:33]
	v_mfma_f32_16x16x32_bf16 v[30:33], v[198:201], v[214:217], v[30:33]
	v_mfma_f32_16x16x32_bf16 v[26:29], v[206:209], v[214:217], v[26:29]
	v_mfma_f32_16x16x32_bf16 v[26:29], v[202:205], v[210:213], v[26:29]
	v_mfma_f32_16x16x32_bf16 v[18:21], v[202:205], v[218:221], v[18:21]
	v_mfma_f32_16x16x32_bf16 v[18:21], v[206:209], v[222:225], v[18:21]
	v_mfma_f32_16x16x32_bf16 v[22:25], v[198:201], v[222:225], v[22:25]
	v_mfma_f32_16x16x32_bf16 v[22:25], v[194:197], v[218:221], v[22:25]
	v_mfma_f32_16x16x32_bf16 v[14:17], v[194:197], v[226:229], v[14:17]
	v_mfma_f32_16x16x32_bf16 v[14:17], v[198:201], v[230:233], v[14:17]
	v_mfma_f32_16x16x32_bf16 v[10:13], v[206:209], v[230:233], v[10:13]
	v_mfma_f32_16x16x32_bf16 v[10:13], v[202:205], v[226:229], v[10:13]
	v_mfma_f32_16x16x32_bf16 v[2:5], v[202:205], v[234:237], v[2:5]
	v_mfma_f32_16x16x32_bf16 v[2:5], v[206:209], v[238:241], v[2:5]
	v_mfma_f32_16x16x32_bf16 v[6:9], v[198:201], v[238:241], v[6:9]
	v_mfma_f32_16x16x32_bf16 v[6:9], v[194:197], v[234:237], v[6:9]
	s_barrier
	v_add_u32_e32 v166, 0x18000, v179
	ds_read_b128 v[162:165], v166
	ds_read_b128 v[182:185], v166 offset:1024
	ds_read_b128 v[186:189], v166 offset:2048
	ds_read_b128 v[190:193], v166 offset:3072
	v_add_u32_e32 v166, 0x1c000, v179
	ds_read_b128 v[194:197], v166
	ds_read_b128 v[198:201], v166 offset:1024
	ds_read_b128 v[202:205], v166 offset:2048
	ds_read_b128 v[206:209], v166 offset:3072
	s_add_i32 s29, s29, 0x80000
	s_mov_b32 m0, s43
	ds_read_b128 v[210:213], v180 offset:32768
	ds_read_b128 v[214:217], v180 offset:33792
	ds_read_b128 v[218:221], v180 offset:34816
	ds_read_b128 v[222:225], v180 offset:35840
	ds_read_b128 v[226:229], v180 offset:36864
	ds_read_b128 v[230:233], v180 offset:37888
	ds_read_b128 v[234:237], v180 offset:38912
	ds_read_b128 v[238:241], v180 offset:39936
	buffer_load_dwordx4 v1, s[4:7], s29 offen lds
	s_mov_b32 m0, s44
	s_nop 0
	buffer_load_dwordx4 v175, s[4:7], s29 offen lds
	s_waitcnt vmcnt(8)
	s_waitcnt lgkmcnt(0)
	s_nop 0
	s_barrier
	v_mfma_f32_16x16x32_bf16 v[126:129], v[162:165], v[210:213], v[126:129]
	v_mfma_f32_16x16x32_bf16 v[126:129], v[182:185], v[214:217], v[126:129]
	v_mfma_f32_16x16x32_bf16 v[122:125], v[190:193], v[214:217], v[122:125]
	v_mfma_f32_16x16x32_bf16 v[122:125], v[186:189], v[210:213], v[122:125]
	v_mfma_f32_16x16x32_bf16 v[114:117], v[186:189], v[218:221], v[114:117]
	v_mfma_f32_16x16x32_bf16 v[114:117], v[190:193], v[222:225], v[114:117]
	v_mfma_f32_16x16x32_bf16 v[118:121], v[182:185], v[222:225], v[118:121]
	v_mfma_f32_16x16x32_bf16 v[118:121], v[162:165], v[218:221], v[118:121]
	v_mfma_f32_16x16x32_bf16 v[110:113], v[162:165], v[226:229], v[110:113]
	v_mfma_f32_16x16x32_bf16 v[110:113], v[182:185], v[230:233], v[110:113]
	v_mfma_f32_16x16x32_bf16 v[106:109], v[190:193], v[230:233], v[106:109]
	v_mfma_f32_16x16x32_bf16 v[106:109], v[186:189], v[226:229], v[106:109]
	v_mfma_f32_16x16x32_bf16 v[98:101], v[186:189], v[234:237], v[98:101]
	v_mfma_f32_16x16x32_bf16 v[98:101], v[190:193], v[238:241], v[98:101]
	v_mfma_f32_16x16x32_bf16 v[102:105], v[182:185], v[238:241], v[102:105]
	v_mfma_f32_16x16x32_bf16 v[102:105], v[162:165], v[234:237], v[102:105]
	v_mfma_f32_16x16x32_bf16 v[94:97], v[194:197], v[210:213], v[94:97]
	v_mfma_f32_16x16x32_bf16 v[94:97], v[198:201], v[214:217], v[94:97]
	v_mfma_f32_16x16x32_bf16 v[90:93], v[206:209], v[214:217], v[90:93]
	v_mfma_f32_16x16x32_bf16 v[90:93], v[202:205], v[210:213], v[90:93]
	v_mfma_f32_16x16x32_bf16 v[82:85], v[202:205], v[218:221], v[82:85]
	v_mfma_f32_16x16x32_bf16 v[82:85], v[206:209], v[222:225], v[82:85]
	v_mfma_f32_16x16x32_bf16 v[86:89], v[198:201], v[222:225], v[86:89]
	v_mfma_f32_16x16x32_bf16 v[86:89], v[194:197], v[218:221], v[86:89]
	v_mfma_f32_16x16x32_bf16 v[78:81], v[194:197], v[226:229], v[78:81]
	v_mfma_f32_16x16x32_bf16 v[78:81], v[198:201], v[230:233], v[78:81]
	v_mfma_f32_16x16x32_bf16 v[74:77], v[206:209], v[230:233], v[74:77]
	v_mfma_f32_16x16x32_bf16 v[74:77], v[202:205], v[226:229], v[74:77]
	v_mfma_f32_16x16x32_bf16 v[66:69], v[202:205], v[234:237], v[66:69]
	v_mfma_f32_16x16x32_bf16 v[66:69], v[206:209], v[238:241], v[66:69]
	v_mfma_f32_16x16x32_bf16 v[70:73], v[198:201], v[238:241], v[70:73]
	v_mfma_f32_16x16x32_bf16 v[70:73], v[194:197], v[234:237], v[70:73]
	s_barrier
	s_mov_b32 m0, s49
	ds_read_b128 v[210:213], v180 offset:49152
	ds_read_b128 v[214:217], v180 offset:50176
	ds_read_b128 v[218:221], v180 offset:51200
	ds_read_b128 v[222:225], v180 offset:52224
	ds_read_b128 v[226:229], v180 offset:53248
	ds_read_b128 v[230:233], v180 offset:54272
	ds_read_b128 v[234:237], v180 offset:55296
	ds_read_b128 v[238:241], v180 offset:56320
	buffer_load_dwordx4 v174, s[8:11], s28 offen lds
	s_mov_b32 m0, s50
	s_add_i32 s27, s27, 0x80080
	buffer_load_dwordx4 v176, s[8:11], s28 offen lds
	s_mov_b32 m0, s53
	s_nop 0
	buffer_load_dwordx4 v174, s[8:11], s27 offen lds
	s_mov_b32 m0, s54
	s_nop 0
	buffer_load_dwordx4 v176, s[8:11], s27 offen lds
	s_mov_b32 m0, s51
	s_nop 0
	buffer_load_dwordx4 v1, s[4:7], s26 offen lds
	s_mov_b32 m0, s52
	s_nop 0
	buffer_load_dwordx4 v175, s[4:7], s26 offen lds
	s_waitcnt vmcnt(8)
	s_waitcnt lgkmcnt(0)
	s_barrier
	v_mfma_f32_16x16x32_bf16 v[62:65], v[162:165], v[210:213], v[62:65]
	v_mfma_f32_16x16x32_bf16 v[62:65], v[182:185], v[214:217], v[62:65]
	v_mfma_f32_16x16x32_bf16 v[58:61], v[190:193], v[214:217], v[58:61]
	v_mfma_f32_16x16x32_bf16 v[58:61], v[186:189], v[210:213], v[58:61]
	v_mfma_f32_16x16x32_bf16 v[50:53], v[186:189], v[218:221], v[50:53]
	v_mfma_f32_16x16x32_bf16 v[50:53], v[190:193], v[222:225], v[50:53]
	v_mfma_f32_16x16x32_bf16 v[54:57], v[182:185], v[222:225], v[54:57]
	v_mfma_f32_16x16x32_bf16 v[54:57], v[162:165], v[218:221], v[54:57]
	v_mfma_f32_16x16x32_bf16 v[46:49], v[162:165], v[226:229], v[46:49]
	v_mfma_f32_16x16x32_bf16 v[46:49], v[182:185], v[230:233], v[46:49]
	v_mfma_f32_16x16x32_bf16 v[42:45], v[190:193], v[230:233], v[42:45]
	v_mfma_f32_16x16x32_bf16 v[42:45], v[186:189], v[226:229], v[42:45]
	v_mfma_f32_16x16x32_bf16 v[34:37], v[186:189], v[234:237], v[34:37]
	v_mfma_f32_16x16x32_bf16 v[34:37], v[190:193], v[238:241], v[34:37]
	v_mfma_f32_16x16x32_bf16 v[38:41], v[182:185], v[238:241], v[38:41]
	v_mfma_f32_16x16x32_bf16 v[38:41], v[162:165], v[234:237], v[38:41]
	v_mfma_f32_16x16x32_bf16 v[30:33], v[194:197], v[210:213], v[30:33]
	v_mfma_f32_16x16x32_bf16 v[30:33], v[198:201], v[214:217], v[30:33]
	v_mfma_f32_16x16x32_bf16 v[26:29], v[206:209], v[214:217], v[26:29]
	v_mfma_f32_16x16x32_bf16 v[26:29], v[202:205], v[210:213], v[26:29]
	v_mfma_f32_16x16x32_bf16 v[18:21], v[202:205], v[218:221], v[18:21]
	v_mfma_f32_16x16x32_bf16 v[18:21], v[206:209], v[222:225], v[18:21]
	v_mfma_f32_16x16x32_bf16 v[22:25], v[198:201], v[222:225], v[22:25]
	v_mfma_f32_16x16x32_bf16 v[22:25], v[194:197], v[218:221], v[22:25]
	v_mfma_f32_16x16x32_bf16 v[14:17], v[194:197], v[226:229], v[14:17]
	v_mfma_f32_16x16x32_bf16 v[14:17], v[198:201], v[230:233], v[14:17]
	v_mfma_f32_16x16x32_bf16 v[10:13], v[206:209], v[230:233], v[10:13]
	v_mfma_f32_16x16x32_bf16 v[10:13], v[202:205], v[226:229], v[10:13]
	v_mfma_f32_16x16x32_bf16 v[2:5], v[202:205], v[234:237], v[2:5]
	v_mfma_f32_16x16x32_bf16 v[2:5], v[206:209], v[238:241], v[2:5]
	v_mfma_f32_16x16x32_bf16 v[6:9], v[198:201], v[238:241], v[6:9]
	v_mfma_f32_16x16x32_bf16 v[6:9], v[194:197], v[234:237], v[6:9]
	s_barrier
	s_add_i32 s10, s65, 2
	s_addk_i32 s64, 0x100
	s_cmp_gt_u32 s65, 29
	s_cbranch_scc1 .LBB0_910
	s_mov_b32 s65, s10
	s_branch .LBB0_869

.LBB0_1029:
	v_add_u32_e32 v152, 0x10000, v138
	v_add_u32_e32 v168, 0x14000, v138
	ds_read_b128 v[140:143], v152
	ds_read_b128 v[144:147], v152 offset:1024
	ds_read_b128 v[148:151], v152 offset:2048
	ds_read_b128 v[152:155], v152 offset:3072
	ds_read_b128 v[156:159], v168
	ds_read_b128 v[160:163], v168 offset:1024
	ds_read_b128 v[164:167], v168 offset:2048
	ds_read_b128 v[168:171], v168 offset:3072
	s_add_i32 s10, s30, s50
	s_add_i32 s51, s25, s50
	s_add_i32 s11, s10, 0x4000
	s_addk_i32 s51, 0x4000
	s_cmp_eq_u32 s50, 0
	s_cselect_b32 s53, s47, s11
	s_cselect_b32 s52, s48, s51
	s_or_b32 s51, s53, 0x80
	s_add_i32 s10, s10, 0x203f80
	s_mov_b32 m0, s41
	ds_read_b128 v[172:175], v139
	ds_read_b128 v[176:179], v139 offset:1024
	ds_read_b128 v[180:183], v139 offset:2048
	ds_read_b128 v[184:187], v139 offset:3072
	ds_read_b128 v[188:191], v139 offset:4096
	ds_read_b128 v[192:195], v139 offset:5120
	ds_read_b128 v[196:199], v139 offset:6144
	ds_read_b128 v[200:203], v139 offset:7168
	buffer_load_dwordx4 v134, s[4:7], s10 offen lds
	s_mov_b32 m0, s42
	s_nop 0
	buffer_load_dwordx4 v136, s[4:7], s10 offen lds
	s_waitcnt vmcnt(8)
	s_waitcnt lgkmcnt(0)
	s_nop 0
	s_barrier
	v_mfma_f32_16x16x32_bf16 v[126:129], v[140:143], v[172:175], v[126:129]
	v_mfma_f32_16x16x32_bf16 v[126:129], v[144:147], v[176:179], v[126:129]
	v_mfma_f32_16x16x32_bf16 v[122:125], v[152:155], v[176:179], v[122:125]
	v_mfma_f32_16x16x32_bf16 v[122:125], v[148:151], v[172:175], v[122:125]
	v_mfma_f32_16x16x32_bf16 v[106:109], v[148:151], v[180:183], v[106:109]
	v_mfma_f32_16x16x32_bf16 v[106:109], v[152:155], v[184:187], v[106:109]
	v_mfma_f32_16x16x32_bf16 v[114:117], v[144:147], v[184:187], v[114:117]
	v_mfma_f32_16x16x32_bf16 v[114:117], v[140:143], v[180:183], v[114:117]
	v_mfma_f32_16x16x32_bf16 v[98:101], v[140:143], v[188:191], v[98:101]
	v_mfma_f32_16x16x32_bf16 v[98:101], v[144:147], v[192:195], v[98:101]
	v_mfma_f32_16x16x32_bf16 v[90:93], v[152:155], v[192:195], v[90:93]
	v_mfma_f32_16x16x32_bf16 v[90:93], v[148:151], v[188:191], v[90:93]
	v_mfma_f32_16x16x32_bf16 v[74:77], v[148:151], v[196:199], v[74:77]
	v_mfma_f32_16x16x32_bf16 v[74:77], v[152:155], v[200:203], v[74:77]
	v_mfma_f32_16x16x32_bf16 v[82:85], v[144:147], v[200:203], v[82:85]
	v_mfma_f32_16x16x32_bf16 v[82:85], v[140:143], v[196:199], v[82:85]
	v_mfma_f32_16x16x32_bf16 v[118:121], v[156:159], v[172:175], v[118:121]
	v_mfma_f32_16x16x32_bf16 v[118:121], v[160:163], v[176:179], v[118:121]
	v_mfma_f32_16x16x32_bf16 v[110:113], v[168:171], v[176:179], v[110:113]
	v_mfma_f32_16x16x32_bf16 v[110:113], v[164:167], v[172:175], v[110:113]
	v_mfma_f32_16x16x32_bf16 v[94:97], v[164:167], v[180:183], v[94:97]
	v_mfma_f32_16x16x32_bf16 v[94:97], v[168:171], v[184:187], v[94:97]
	v_mfma_f32_16x16x32_bf16 v[102:105], v[160:163], v[184:187], v[102:105]
	v_mfma_f32_16x16x32_bf16 v[102:105], v[156:159], v[180:183], v[102:105]
	v_mfma_f32_16x16x32_bf16 v[86:89], v[156:159], v[188:191], v[86:89]
	v_mfma_f32_16x16x32_bf16 v[86:89], v[160:163], v[192:195], v[86:89]
	v_mfma_f32_16x16x32_bf16 v[78:81], v[168:171], v[192:195], v[78:81]
	v_mfma_f32_16x16x32_bf16 v[78:81], v[164:167], v[188:191], v[78:81]
	v_mfma_f32_16x16x32_bf16 v[66:69], v[164:167], v[196:199], v[66:69]
	v_mfma_f32_16x16x32_bf16 v[66:69], v[168:171], v[200:203], v[66:69]
	v_mfma_f32_16x16x32_bf16 v[70:73], v[160:163], v[200:203], v[70:73]
	v_mfma_f32_16x16x32_bf16 v[70:73], v[156:159], v[196:199], v[70:73]
	s_barrier
	s_mov_b32 m0, s24
	s_mov_b32 s10, s6
	s_mov_b32 s11, s7
	ds_read_b128 v[172:175], v139 offset:16384
	ds_read_b128 v[176:179], v139 offset:17408
	ds_read_b128 v[180:183], v139 offset:18432
	ds_read_b128 v[184:187], v139 offset:19456
	ds_read_b128 v[188:191], v139 offset:20480
	ds_read_b128 v[192:195], v139 offset:21504
	ds_read_b128 v[196:199], v139 offset:22528
	ds_read_b128 v[200:203], v139 offset:23552
	buffer_load_dwordx4 v135, s[8:11], s52 offen lds
	s_mov_b32 m0, s26
	s_add_i32 s54, s52, 0x200000
	buffer_load_dwordx4 v137, s[8:11], s52 offen lds
	s_mov_b32 m0, s27
	s_nop 0
	buffer_load_dwordx4 v135, s[8:11], s54 offen lds
	s_mov_b32 m0, s28
	s_nop 0
	buffer_load_dwordx4 v137, s[8:11], s54 offen lds
	s_mov_b32 m0, s23
	s_nop 0
	buffer_load_dwordx4 v134, s[4:7], s53 offen lds
	s_mov_b32 m0, s29
	s_nop 0
	buffer_load_dwordx4 v136, s[4:7], s53 offen lds
	s_waitcnt vmcnt(8)
	s_waitcnt lgkmcnt(0)
	s_barrier
	v_mfma_f32_16x16x32_bf16 v[62:65], v[140:143], v[172:175], v[62:65]
	v_mfma_f32_16x16x32_bf16 v[62:65], v[144:147], v[176:179], v[62:65]
	v_mfma_f32_16x16x32_bf16 v[58:61], v[152:155], v[176:179], v[58:61]
	v_mfma_f32_16x16x32_bf16 v[58:61], v[148:151], v[172:175], v[58:61]
	v_mfma_f32_16x16x32_bf16 v[42:45], v[148:151], v[180:183], v[42:45]
	v_mfma_f32_16x16x32_bf16 v[42:45], v[152:155], v[184:187], v[42:45]
	v_mfma_f32_16x16x32_bf16 v[50:53], v[144:147], v[184:187], v[50:53]
	v_mfma_f32_16x16x32_bf16 v[50:53], v[140:143], v[180:183], v[50:53]
	v_mfma_f32_16x16x32_bf16 v[34:37], v[140:143], v[188:191], v[34:37]
	v_mfma_f32_16x16x32_bf16 v[34:37], v[144:147], v[192:195], v[34:37]
	v_mfma_f32_16x16x32_bf16 v[26:29], v[152:155], v[192:195], v[26:29]
	v_mfma_f32_16x16x32_bf16 v[26:29], v[148:151], v[188:191], v[26:29]
	v_mfma_f32_16x16x32_bf16 v[10:13], v[148:151], v[196:199], v[10:13]
	v_mfma_f32_16x16x32_bf16 v[10:13], v[152:155], v[200:203], v[10:13]
	v_mfma_f32_16x16x32_bf16 v[18:21], v[144:147], v[200:203], v[18:21]
	v_mfma_f32_16x16x32_bf16 v[18:21], v[140:143], v[196:199], v[18:21]
	v_mfma_f32_16x16x32_bf16 v[54:57], v[156:159], v[172:175], v[54:57]
	v_mfma_f32_16x16x32_bf16 v[54:57], v[160:163], v[176:179], v[54:57]
	v_mfma_f32_16x16x32_bf16 v[46:49], v[168:171], v[176:179], v[46:49]
	v_mfma_f32_16x16x32_bf16 v[46:49], v[164:167], v[172:175], v[46:49]
	v_mfma_f32_16x16x32_bf16 v[30:33], v[164:167], v[180:183], v[30:33]
	v_mfma_f32_16x16x32_bf16 v[30:33], v[168:171], v[184:187], v[30:33]
	v_mfma_f32_16x16x32_bf16 v[38:41], v[160:163], v[184:187], v[38:41]
	v_mfma_f32_16x16x32_bf16 v[38:41], v[156:159], v[180:183], v[38:41]
	v_mfma_f32_16x16x32_bf16 v[22:25], v[156:159], v[188:191], v[22:25]
	v_mfma_f32_16x16x32_bf16 v[22:25], v[160:163], v[192:195], v[22:25]
	v_mfma_f32_16x16x32_bf16 v[14:17], v[168:171], v[192:195], v[14:17]
	v_mfma_f32_16x16x32_bf16 v[14:17], v[164:167], v[188:191], v[14:17]
	v_mfma_f32_16x16x32_bf16 v[2:5], v[164:167], v[196:199], v[2:5]
	v_mfma_f32_16x16x32_bf16 v[2:5], v[168:171], v[200:203], v[2:5]
	v_mfma_f32_16x16x32_bf16 v[6:9], v[160:163], v[200:203], v[6:9]
	v_mfma_f32_16x16x32_bf16 v[6:9], v[156:159], v[196:199], v[6:9]
	s_barrier
	v_add_u32_e32 v152, 0x18000, v138
	v_add_u32_e32 v168, 0x1c000, v138
	ds_read_b128 v[140:143], v152
	ds_read_b128 v[144:147], v152 offset:1024
	ds_read_b128 v[148:151], v152 offset:2048
	ds_read_b128 v[152:155], v152 offset:3072
	ds_read_b128 v[156:159], v168
	ds_read_b128 v[160:163], v168 offset:1024
	ds_read_b128 v[164:167], v168 offset:2048
	ds_read_b128 v[168:171], v168 offset:3072
	s_add_i32 s53, s53, 0x200000
	s_mov_b32 m0, s31
	ds_read_b128 v[172:175], v139 offset:32768
	ds_read_b128 v[176:179], v139 offset:33792
	ds_read_b128 v[180:183], v139 offset:34816
	ds_read_b128 v[184:187], v139 offset:35840
	ds_read_b128 v[188:191], v139 offset:36864
	ds_read_b128 v[192:195], v139 offset:37888
	ds_read_b128 v[196:199], v139 offset:38912
	ds_read_b128 v[200:203], v139 offset:39936
	buffer_load_dwordx4 v134, s[4:7], s53 offen lds
	s_mov_b32 m0, s33
	s_nop 0
	buffer_load_dwordx4 v136, s[4:7], s53 offen lds
	s_waitcnt vmcnt(8)
	s_waitcnt lgkmcnt(0)
	s_nop 0
	s_barrier
	v_mfma_f32_16x16x32_bf16 v[126:129], v[140:143], v[172:175], v[126:129]
	v_mfma_f32_16x16x32_bf16 v[126:129], v[144:147], v[176:179], v[126:129]
	v_mfma_f32_16x16x32_bf16 v[122:125], v[152:155], v[176:179], v[122:125]
	v_mfma_f32_16x16x32_bf16 v[122:125], v[148:151], v[172:175], v[122:125]
	v_mfma_f32_16x16x32_bf16 v[106:109], v[148:151], v[180:183], v[106:109]
	v_mfma_f32_16x16x32_bf16 v[106:109], v[152:155], v[184:187], v[106:109]
	v_mfma_f32_16x16x32_bf16 v[114:117], v[144:147], v[184:187], v[114:117]
	v_mfma_f32_16x16x32_bf16 v[114:117], v[140:143], v[180:183], v[114:117]
	v_mfma_f32_16x16x32_bf16 v[98:101], v[140:143], v[188:191], v[98:101]
	v_mfma_f32_16x16x32_bf16 v[98:101], v[144:147], v[192:195], v[98:101]
	v_mfma_f32_16x16x32_bf16 v[90:93], v[152:155], v[192:195], v[90:93]
	v_mfma_f32_16x16x32_bf16 v[90:93], v[148:151], v[188:191], v[90:93]
	v_mfma_f32_16x16x32_bf16 v[74:77], v[148:151], v[196:199], v[74:77]
	v_mfma_f32_16x16x32_bf16 v[74:77], v[152:155], v[200:203], v[74:77]
	v_mfma_f32_16x16x32_bf16 v[82:85], v[144:147], v[200:203], v[82:85]
	v_mfma_f32_16x16x32_bf16 v[82:85], v[140:143], v[196:199], v[82:85]
	v_mfma_f32_16x16x32_bf16 v[118:121], v[156:159], v[172:175], v[118:121]
	v_mfma_f32_16x16x32_bf16 v[118:121], v[160:163], v[176:179], v[118:121]
	v_mfma_f32_16x16x32_bf16 v[110:113], v[168:171], v[176:179], v[110:113]
	v_mfma_f32_16x16x32_bf16 v[110:113], v[164:167], v[172:175], v[110:113]
	v_mfma_f32_16x16x32_bf16 v[94:97], v[164:167], v[180:183], v[94:97]
	v_mfma_f32_16x16x32_bf16 v[94:97], v[168:171], v[184:187], v[94:97]
	v_mfma_f32_16x16x32_bf16 v[102:105], v[160:163], v[184:187], v[102:105]
	v_mfma_f32_16x16x32_bf16 v[102:105], v[156:159], v[180:183], v[102:105]
	v_mfma_f32_16x16x32_bf16 v[86:89], v[156:159], v[188:191], v[86:89]
	v_mfma_f32_16x16x32_bf16 v[86:89], v[160:163], v[192:195], v[86:89]
	v_mfma_f32_16x16x32_bf16 v[78:81], v[168:171], v[192:195], v[78:81]
	v_mfma_f32_16x16x32_bf16 v[78:81], v[164:167], v[188:191], v[78:81]
	v_mfma_f32_16x16x32_bf16 v[66:69], v[164:167], v[196:199], v[66:69]
	v_mfma_f32_16x16x32_bf16 v[66:69], v[168:171], v[200:203], v[66:69]
	v_mfma_f32_16x16x32_bf16 v[70:73], v[160:163], v[200:203], v[70:73]
	v_mfma_f32_16x16x32_bf16 v[70:73], v[156:159], v[196:199], v[70:73]
	s_barrier
	s_mov_b32 m0, s34
	s_or_b32 s53, s52, 0x80
	ds_read_b128 v[172:175], v139 offset:49152
	ds_read_b128 v[176:179], v139 offset:50176
	ds_read_b128 v[180:183], v139 offset:51200
	ds_read_b128 v[184:187], v139 offset:52224
	ds_read_b128 v[188:191], v139 offset:53248
	ds_read_b128 v[192:195], v139 offset:54272
	ds_read_b128 v[196:199], v139 offset:55296
	ds_read_b128 v[200:203], v139 offset:56320
	buffer_load_dwordx4 v135, s[8:11], s53 offen lds
	s_mov_b32 m0, s35
	s_add_i32 s52, s52, 0x200080
	buffer_load_dwordx4 v137, s[8:11], s53 offen lds
	s_mov_b32 m0, s39
	s_nop 0
	buffer_load_dwordx4 v135, s[8:11], s52 offen lds
	s_mov_b32 m0, s40
	s_nop 0
	buffer_load_dwordx4 v137, s[8:11], s52 offen lds
	s_mov_b32 m0, s37
	s_nop 0
	buffer_load_dwordx4 v134, s[4:7], s51 offen lds
	s_mov_b32 m0, s38
	s_nop 0
	buffer_load_dwordx4 v136, s[4:7], s51 offen lds
	s_waitcnt vmcnt(8)
	s_waitcnt lgkmcnt(0)
	s_barrier
	v_mfma_f32_16x16x32_bf16 v[62:65], v[140:143], v[172:175], v[62:65]
	v_mfma_f32_16x16x32_bf16 v[62:65], v[144:147], v[176:179], v[62:65]
	v_mfma_f32_16x16x32_bf16 v[58:61], v[152:155], v[176:179], v[58:61]
	v_mfma_f32_16x16x32_bf16 v[58:61], v[148:151], v[172:175], v[58:61]
	v_mfma_f32_16x16x32_bf16 v[42:45], v[148:151], v[180:183], v[42:45]
	v_mfma_f32_16x16x32_bf16 v[42:45], v[152:155], v[184:187], v[42:45]
	v_mfma_f32_16x16x32_bf16 v[50:53], v[144:147], v[184:187], v[50:53]
	v_mfma_f32_16x16x32_bf16 v[50:53], v[140:143], v[180:183], v[50:53]
	v_mfma_f32_16x16x32_bf16 v[34:37], v[140:143], v[188:191], v[34:37]
	v_mfma_f32_16x16x32_bf16 v[34:37], v[144:147], v[192:195], v[34:37]
	v_mfma_f32_16x16x32_bf16 v[26:29], v[152:155], v[192:195], v[26:29]
	v_mfma_f32_16x16x32_bf16 v[26:29], v[148:151], v[188:191], v[26:29]
	v_mfma_f32_16x16x32_bf16 v[10:13], v[148:151], v[196:199], v[10:13]
	v_mfma_f32_16x16x32_bf16 v[10:13], v[152:155], v[200:203], v[10:13]
	v_mfma_f32_16x16x32_bf16 v[18:21], v[144:147], v[200:203], v[18:21]
	v_mfma_f32_16x16x32_bf16 v[18:21], v[140:143], v[196:199], v[18:21]
	v_mfma_f32_16x16x32_bf16 v[54:57], v[156:159], v[172:175], v[54:57]
	v_mfma_f32_16x16x32_bf16 v[54:57], v[160:163], v[176:179], v[54:57]
	v_mfma_f32_16x16x32_bf16 v[46:49], v[168:171], v[176:179], v[46:49]
	v_mfma_f32_16x16x32_bf16 v[46:49], v[164:167], v[172:175], v[46:49]
	v_mfma_f32_16x16x32_bf16 v[30:33], v[164:167], v[180:183], v[30:33]
	v_mfma_f32_16x16x32_bf16 v[30:33], v[168:171], v[184:187], v[30:33]
	v_mfma_f32_16x16x32_bf16 v[38:41], v[160:163], v[184:187], v[38:41]
	v_mfma_f32_16x16x32_bf16 v[38:41], v[156:159], v[180:183], v[38:41]
	v_mfma_f32_16x16x32_bf16 v[22:25], v[156:159], v[188:191], v[22:25]
	v_mfma_f32_16x16x32_bf16 v[22:25], v[160:163], v[192:195], v[22:25]
	v_mfma_f32_16x16x32_bf16 v[14:17], v[168:171], v[192:195], v[14:17]
	v_mfma_f32_16x16x32_bf16 v[14:17], v[164:167], v[188:191], v[14:17]
	v_mfma_f32_16x16x32_bf16 v[2:5], v[164:167], v[196:199], v[2:5]
	v_mfma_f32_16x16x32_bf16 v[2:5], v[168:171], v[200:203], v[2:5]
	v_mfma_f32_16x16x32_bf16 v[6:9], v[160:163], v[200:203], v[6:9]
	v_mfma_f32_16x16x32_bf16 v[6:9], v[156:159], v[196:199], v[6:9]
	s_barrier
	s_add_i32 s49, s49, 2
	s_addk_i32 s50, 0x100
	s_cmpk_gt_u32 s49, 0x7d
	s_cbranch_scc0 .LBB0_1029
	s_andn2_b64 vcc, exec, s[2:3]
	s_cbranch_vccnz .LBB0_1021
	v_mov_b32_e32 v2, 0
	s_mov_b32 s17, s44
	s_mov_b32 s14, s45
	s_mov_b32 s25, s46
	s_mov_b32 s30, s13
	s_mov_b32 s43, s12
	v_mov_b32_e32 v3, v2
	v_mov_b32_e32 v4, v2
	v_mov_b32_e32 v5, v2
	v_mov_b32_e32 v6, v2
	v_mov_b32_e32 v7, v2
	v_mov_b32_e32 v8, v2
	v_mov_b32_e32 v9, v2
	v_mov_b32_e32 v14, v2
	v_mov_b32_e32 v15, v2
	v_mov_b32_e32 v16, v2
	v_mov_b32_e32 v17, v2
	v_mov_b32_e32 v22, v2
	v_mov_b32_e32 v23, v2
	v_mov_b32_e32 v24, v2
	v_mov_b32_e32 v25, v2
	v_mov_b32_e32 v30, v2
	v_mov_b32_e32 v31, v2
	v_mov_b32_e32 v32, v2
	v_mov_b32_e32 v33, v2
	v_mov_b32_e32 v38, v2
	v_mov_b32_e32 v39, v2
	v_mov_b32_e32 v40, v2
	v_mov_b32_e32 v41, v2
	v_mov_b32_e32 v46, v2
	v_mov_b32_e32 v47, v2
	v_mov_b32_e32 v48, v2
	v_mov_b32_e32 v49, v2
	v_mov_b32_e32 v54, v2
	v_mov_b32_e32 v55, v2
	v_mov_b32_e32 v56, v2
	v_mov_b32_e32 v57, v2
	v_mov_b32_e32 v10, v2
	v_mov_b32_e32 v11, v2
	v_mov_b32_e32 v12, v2
	v_mov_b32_e32 v13, v2
	v_mov_b32_e32 v18, v2
	v_mov_b32_e32 v19, v2
	v_mov_b32_e32 v20, v2
	v_mov_b32_e32 v21, v2
	v_mov_b32_e32 v26, v2
	v_mov_b32_e32 v27, v2
	v_mov_b32_e32 v28, v2
	v_mov_b32_e32 v29, v2
	v_mov_b32_e32 v34, v2
	v_mov_b32_e32 v35, v2
	v_mov_b32_e32 v36, v2
	v_mov_b32_e32 v37, v2
	v_mov_b32_e32 v42, v2
	v_mov_b32_e32 v43, v2
	v_mov_b32_e32 v44, v2
	v_mov_b32_e32 v45, v2
	v_mov_b32_e32 v50, v2
	v_mov_b32_e32 v51, v2
	v_mov_b32_e32 v52, v2
	v_mov_b32_e32 v53, v2
	v_mov_b32_e32 v58, v2
	v_mov_b32_e32 v59, v2
	v_mov_b32_e32 v60, v2
	v_mov_b32_e32 v61, v2
	v_mov_b32_e32 v62, v2
	v_mov_b32_e32 v63, v2
	v_mov_b32_e32 v64, v2
	v_mov_b32_e32 v65, v2
	v_mov_b32_e32 v66, v2
	v_mov_b32_e32 v67, v2
	v_mov_b32_e32 v68, v2
	v_mov_b32_e32 v69, v2
	v_mov_b32_e32 v70, v2
	v_mov_b32_e32 v71, v2
	v_mov_b32_e32 v72, v2
	v_mov_b32_e32 v73, v2
	v_mov_b32_e32 v78, v2
	v_mov_b32_e32 v79, v2
	v_mov_b32_e32 v80, v2
	v_mov_b32_e32 v81, v2
	v_mov_b32_e32 v86, v2
	v_mov_b32_e32 v87, v2
	v_mov_b32_e32 v88, v2
	v_mov_b32_e32 v89, v2
	v_mov_b32_e32 v94, v2
	v_mov_b32_e32 v95, v2
	v_mov_b32_e32 v96, v2
	v_mov_b32_e32 v97, v2
	v_mov_b32_e32 v102, v2
	v_mov_b32_e32 v103, v2
	v_mov_b32_e32 v104, v2
	v_mov_b32_e32 v105, v2
	v_mov_b32_e32 v110, v2
	v_mov_b32_e32 v111, v2
	v_mov_b32_e32 v112, v2
	v_mov_b32_e32 v113, v2
	v_mov_b32_e32 v118, v2
	v_mov_b32_e32 v119, v2
	v_mov_b32_e32 v120, v2
	v_mov_b32_e32 v121, v2
	v_mov_b32_e32 v74, v2
	v_mov_b32_e32 v75, v2
	v_mov_b32_e32 v76, v2
	v_mov_b32_e32 v77, v2
	v_mov_b32_e32 v82, v2
	v_mov_b32_e32 v83, v2
	v_mov_b32_e32 v84, v2
	v_mov_b32_e32 v85, v2
	v_mov_b32_e32 v90, v2
	v_mov_b32_e32 v91, v2
	v_mov_b32_e32 v92, v2
	v_mov_b32_e32 v93, v2
	v_mov_b32_e32 v98, v2
	v_mov_b32_e32 v99, v2
	v_mov_b32_e32 v100, v2
	v_mov_b32_e32 v101, v2
	v_mov_b32_e32 v106, v2
	v_mov_b32_e32 v107, v2
	v_mov_b32_e32 v108, v2
	v_mov_b32_e32 v109, v2
	v_mov_b32_e32 v114, v2
	v_mov_b32_e32 v115, v2
	v_mov_b32_e32 v116, v2
	v_mov_b32_e32 v117, v2
	v_mov_b32_e32 v122, v2
	v_mov_b32_e32 v123, v2
	v_mov_b32_e32 v124, v2
	v_mov_b32_e32 v125, v2
	v_mov_b32_e32 v126, v2
	v_mov_b32_e32 v127, v2
	v_mov_b32_e32 v128, v2
	v_mov_b32_e32 v129, v2
	s_branch .LBB0_1021
